# prep gate blocks: the 34 second-stage loads (sk_w2/sv_w2 columns, biases) issued during the second MFMA round into free registers
# speedup vs baseline: 1.0263x; 1.0011x over previous
.LBB13_3:
	s_cmpk_lt_i32 s2, 0x100
	v_lshrrev_b32_e32 v1, 6, v0
	v_and_b32_e32 v36, 63, v0
	s_cbranch_scc0 .LBB13_5
	v_bfe_u32 v13, v0, 4, 2
	v_and_b32_e32 v12, 15, v0
	s_lshl_b32 s22, s2, 4
	v_lshlrev_b32_e32 v2, 3, v13
	v_lshl_or_b32 v14, v1, 8, v2
	v_or_b32_e32 v2, s22, v12
	s_load_dwordx8 s[4:11], s[0:1], 0x30
	s_load_dwordx2 s[26:27], s[0:1], 0x60
	v_ashrrev_i32_e32 v3, 31, v2
	v_lshlrev_b64 v[2:3], 12, v[2:3]
	s_waitcnt lgkmcnt(0)
	v_lshl_add_u64 v[2:3], s[20:21], 0, v[2:3]
	v_lshlrev_b32_e32 v18, 2, v14
	v_mov_b32_e32 v19, 0
	v_lshl_or_b32 v14, v14, 4, v12
	v_lshl_add_u64 v[10:11], v[2:3], 0, v[18:19]
	v_subrev_u32_e32 v108, s20, v10
	v_lshrrev_b32_e32 v108, 1, v108
	global_load_dwordx4 v[116:119], v[10:11], off offset:528 nt
	global_load_dwordx4 v[112:115], v[10:11], off offset:512 nt
	global_load_dwordx4 v[124:127], v[10:11], off offset:656 nt
	global_load_dwordx4 v[120:123], v[10:11], off offset:640 nt
	global_load_dwordx4 v[132:135], v[10:11], off offset:784 nt
	global_load_dwordx4 v[128:131], v[10:11], off offset:768 nt
	global_load_dwordx4 v[140:143], v[10:11], off offset:912 nt
	global_load_dwordx4 v[136:139], v[10:11], off offset:896 nt
	global_load_dwordx4 v[148:151], v[10:11], off offset:400 nt
	global_load_dwordx4 v[144:147], v[10:11], off offset:384 nt
	v_or_b32_e32 v18, 0x200, v14
	v_lshlrev_b64 v[16:17], 2, v[18:19]
	v_lshlrev_b32_e32 v15, 2, v14
	v_lshl_add_u64 v[28:29], s[4:5], 0, v[16:17]
	v_lshl_add_u64 v[16:17], s[10:11], 0, v[16:17]
	v_or_b32_e32 v18, 0x400, v14
	global_load_dwordx4 v[2:5], v[10:11], off offset:16 nt
	global_load_dwordx4 v[6:9], v[10:11], off nt
	global_load_dword v37, v15, s[4:5]
	global_load_dword v48, v15, s[10:11]
	global_load_dword v49, v15, s[4:5] offset:64
	global_load_dword v50, v15, s[10:11] offset:64
	global_load_dword v51, v15, s[4:5] offset:128
	global_load_dword v52, v15, s[10:11] offset:128
	global_load_dword v53, v15, s[4:5] offset:192
	global_load_dword v54, v15, s[10:11] offset:192
	global_load_dword v55, v15, s[4:5] offset:256
	global_load_dword v56, v15, s[10:11] offset:256
	global_load_dword v57, v15, s[4:5] offset:320
	global_load_dword v58, v15, s[10:11] offset:320
	global_load_dword v59, v15, s[4:5] offset:384
	global_load_dword v60, v15, s[10:11] offset:384
	global_load_dword v61, v15, s[4:5] offset:448
	global_load_dword v62, v15, s[10:11] offset:448
	global_load_dwordx4 v[20:23], v[10:11], off offset:144 nt
	global_load_dwordx4 v[24:27], v[10:11], off offset:128 nt
	global_load_dword v63, v[28:29], off
	global_load_dword v64, v[16:17], off
	global_load_dword v65, v15, s[4:5] offset:2112
	global_load_dword v66, v15, s[10:11] offset:2112
	global_load_dword v67, v15, s[4:5] offset:2176
	global_load_dword v68, v15, s[10:11] offset:2176
	global_load_dword v69, v15, s[4:5] offset:2240
	global_load_dword v70, v15, s[10:11] offset:2240
	global_load_dword v71, v15, s[4:5] offset:2304
	global_load_dword v72, v15, s[10:11] offset:2304
	global_load_dword v73, v15, s[4:5] offset:2368
	global_load_dword v74, v15, s[10:11] offset:2368
	global_load_dword v75, v15, s[4:5] offset:2432
	global_load_dword v76, v15, s[10:11] offset:2432
	global_load_dword v77, v15, s[4:5] offset:2496
	global_load_dword v78, v15, s[10:11] offset:2496
	s_nop 0
	global_load_dwordx4 v[28:31], v[10:11], off offset:272 nt
	global_load_dwordx4 v[32:35], v[10:11], off offset:256 nt
	v_lshlrev_b64 v[16:17], 2, v[18:19]
	v_lshl_add_u64 v[38:39], s[4:5], 0, v[16:17]
	v_lshl_add_u64 v[16:17], s[10:11], 0, v[16:17]
	v_or_b32_e32 v18, 0x410, v14
	global_load_dword v79, v[16:17], off
	v_lshlrev_b64 v[16:17], 2, v[18:19]
	global_load_dword v15, v[38:39], off
	v_lshl_add_u64 v[38:39], s[4:5], 0, v[16:17]
	v_lshl_add_u64 v[16:17], s[10:11], 0, v[16:17]
	v_or_b32_e32 v18, 0x420, v14
	global_load_dword v81, v[16:17], off
	v_lshlrev_b64 v[16:17], 2, v[18:19]
	global_load_dword v80, v[38:39], off
	v_lshl_add_u64 v[38:39], s[4:5], 0, v[16:17]
	v_lshl_add_u64 v[16:17], s[10:11], 0, v[16:17]
	v_or_b32_e32 v18, 0x430, v14
	global_load_dword v83, v[16:17], off
	v_lshlrev_b64 v[16:17], 2, v[18:19]
	global_load_dword v82, v[38:39], off
	v_lshl_add_u64 v[38:39], s[4:5], 0, v[16:17]
	v_lshl_add_u64 v[16:17], s[10:11], 0, v[16:17]
	v_or_b32_e32 v18, 0x440, v14
	global_load_dword v85, v[16:17], off
	v_lshlrev_b64 v[16:17], 2, v[18:19]
	global_load_dword v84, v[38:39], off
	v_lshl_add_u64 v[38:39], s[4:5], 0, v[16:17]
	v_lshl_add_u64 v[16:17], s[10:11], 0, v[16:17]
	v_or_b32_e32 v18, 0x450, v14
	global_load_dword v87, v[16:17], off
	v_lshlrev_b64 v[16:17], 2, v[18:19]
	global_load_dword v86, v[38:39], off
	v_lshl_add_u64 v[38:39], s[4:5], 0, v[16:17]
	v_lshl_add_u64 v[16:17], s[10:11], 0, v[16:17]
	v_or_b32_e32 v18, 0x460, v14
	global_load_dword v89, v[16:17], off
	v_lshlrev_b64 v[16:17], 2, v[18:19]
	global_load_dword v88, v[38:39], off
	v_lshl_add_u64 v[38:39], s[4:5], 0, v[16:17]
	v_lshl_add_u64 v[16:17], s[10:11], 0, v[16:17]
	v_or_b32_e32 v18, 0x470, v14
	global_load_dword v91, v[16:17], off
	v_lshlrev_b64 v[16:17], 2, v[18:19]
	global_load_dword v90, v[38:39], off
	v_lshl_add_u64 v[38:39], s[4:5], 0, v[16:17]
	v_lshl_add_u64 v[16:17], s[10:11], 0, v[16:17]
	v_or_b32_e32 v18, 0x600, v14
	global_load_dword v92, v[38:39], off
	global_load_dword v93, v[16:17], off
	s_nop 0
	v_lshlrev_b64 v[16:17], 2, v[18:19]
	v_lshl_add_u64 v[46:47], s[4:5], 0, v[16:17]
	v_lshl_add_u64 v[16:17], s[10:11], 0, v[16:17]
	v_or_b32_e32 v18, 0x610, v14
	global_load_dword v95, v[16:17], off
	v_lshlrev_b64 v[16:17], 2, v[18:19]
	global_load_dword v94, v[46:47], off
	v_lshl_add_u64 v[46:47], s[4:5], 0, v[16:17]
	v_lshl_add_u64 v[16:17], s[10:11], 0, v[16:17]
	v_or_b32_e32 v18, 0x620, v14
	global_load_dword v97, v[16:17], off
	v_lshlrev_b64 v[16:17], 2, v[18:19]
	global_load_dword v96, v[46:47], off
	v_lshl_add_u64 v[46:47], s[4:5], 0, v[16:17]
	v_lshl_add_u64 v[16:17], s[10:11], 0, v[16:17]
	v_or_b32_e32 v18, 0x630, v14
	global_load_dword v99, v[16:17], off
	v_lshlrev_b64 v[16:17], 2, v[18:19]
	global_load_dword v98, v[46:47], off
	v_lshl_add_u64 v[46:47], s[4:5], 0, v[16:17]
	v_lshl_add_u64 v[16:17], s[10:11], 0, v[16:17]
	v_or_b32_e32 v18, 0x640, v14
	global_load_dword v101, v[16:17], off
	v_lshlrev_b64 v[16:17], 2, v[18:19]
	global_load_dword v100, v[46:47], off
	v_lshl_add_u64 v[46:47], s[4:5], 0, v[16:17]
	v_lshl_add_u64 v[16:17], s[10:11], 0, v[16:17]
	v_or_b32_e32 v18, 0x650, v14
	global_load_dword v103, v[16:17], off
	v_lshlrev_b64 v[16:17], 2, v[18:19]
	global_load_dword v102, v[46:47], off
	v_lshl_add_u64 v[46:47], s[4:5], 0, v[16:17]
	v_lshl_add_u64 v[16:17], s[10:11], 0, v[16:17]
	v_or_b32_e32 v18, 0x660, v14
	global_load_dword v105, v[16:17], off
	v_lshlrev_b64 v[16:17], 2, v[18:19]
	global_load_dword v104, v[46:47], off
	v_lshl_add_u64 v[46:47], s[4:5], 0, v[16:17]
	v_lshl_add_u64 v[16:17], s[10:11], 0, v[16:17]
	v_or_b32_e32 v18, 0x670, v14
	global_load_dword v107, v[16:17], off
	v_lshlrev_b64 v[16:17], 2, v[18:19]
	global_load_dword v106, v[46:47], off
	v_lshl_add_u64 v[46:47], s[4:5], 0, v[16:17]
	v_lshl_add_u64 v[16:17], s[10:11], 0, v[16:17]
	global_load_dword v18, v[46:47], off
	s_mov_b32 s23, 0
	global_load_dword v16, v[16:17], off
	s_load_dwordx2 s[24:25], s[0:1], 0x88
	s_load_dwordx4 s[12:15], s[0:1], 0x78
	s_load_dwordx4 s[16:19], s[0:1], 0x50
	s_waitcnt vmcnt(60)
	v_cvt_pk_f16_f32 v6, v6, v7
	v_cvt_pk_f16_f32 v7, v8, v9
	v_cvt_pk_f16_f32 v8, v2, v3
	v_cvt_pk_f16_f32 v9, v4, v5
	v_cvt_pk_f16_f32 v2, v37, v49
	v_cvt_pk_f16_f32 v3, v51, v53
	s_waitcnt vmcnt(57)
	v_cvt_pk_f16_f32 v4, v55, v57
	s_waitcnt vmcnt(53)
	v_cvt_pk_f16_f32 v5, v59, v61
	v_cvt_pk_f16_f32 v46, v48, v50
	v_cvt_pk_f16_f32 v47, v52, v54
	v_mfma_f32_16x16x32_f16 a[0:3], v[6:9], v[2:5], 0
	global_store_dwordx4 v108, v[6:9], s[26:27] offset:0
	v_cvt_pk_f16_f32 v48, v56, v58
	s_waitcnt vmcnt(53)
	v_cvt_pk_f16_f32 v49, v60, v62
	s_waitcnt vmcnt(51)
	v_cvt_pk_f16_f32 v2, v24, v25
	v_cvt_pk_f16_f32 v3, v26, v27
	v_cvt_pk_f16_f32 v4, v20, v21
	v_cvt_pk_f16_f32 v5, v22, v23
	v_mfma_f32_16x16x32_f16 a[4:7], v[6:9], v[46:49], 0
	s_waitcnt vmcnt(48)
	v_cvt_pk_f16_f32 v6, v63, v65
	s_waitcnt vmcnt(47)
	v_cvt_pk_f16_f32 v20, v64, v66
	s_waitcnt vmcnt(44)
	v_cvt_pk_f16_f32 v7, v67, v69
	s_waitcnt vmcnt(40)
	v_cvt_pk_f16_f32 v8, v71, v73
	s_waitcnt vmcnt(36)
	v_cvt_pk_f16_f32 v9, v75, v77
	v_cvt_pk_f16_f32 v21, v68, v70
	v_cvt_pk_f16_f32 v22, v72, v74
	s_waitcnt vmcnt(35)
	v_cvt_pk_f16_f32 v23, v76, v78
	v_mfma_f32_16x16x32_f16 a[0:3], v[2:5], v[6:9], a[0:3]
	global_store_dwordx4 v108, v[2:5], s[26:27] offset:64
	s_waitcnt vmcnt(30)
	v_cvt_pk_f16_f32 v6, v15, v80
	s_waitcnt vmcnt(26)
	v_cvt_pk_f16_f32 v7, v82, v84
	s_waitcnt vmcnt(22)
	v_cvt_pk_f16_f32 v8, v86, v88
	v_mfma_f32_16x16x32_f16 a[4:7], v[2:5], v[20:23], a[4:7]
	v_cvt_pk_f16_f32 v2, v32, v33
	v_cvt_pk_f16_f32 v3, v34, v35
	v_cvt_pk_f16_f32 v4, v28, v29
	v_cvt_pk_f16_f32 v5, v30, v31
	v_cvt_pk_f16_f32 v20, v79, v81
	s_waitcnt vmcnt(19)
	v_cvt_pk_f16_f32 v9, v90, v92
	v_cvt_pk_f16_f32 v21, v83, v85
	v_cvt_pk_f16_f32 v22, v87, v89
	s_waitcnt vmcnt(18)
	v_cvt_pk_f16_f32 v23, v91, v93
	v_mfma_f32_16x16x32_f16 a[0:3], v[2:5], v[6:9], a[0:3]
	global_store_dwordx4 v108, v[2:5], s[26:27] offset:128
	s_waitcnt vmcnt(15)
	v_cvt_pk_f16_f32 v6, v94, v96
	s_waitcnt vmcnt(11)
	v_cvt_pk_f16_f32 v7, v98, v100
	s_waitcnt vmcnt(7)
	v_cvt_pk_f16_f32 v8, v102, v104
	v_mfma_f32_16x16x32_f16 a[8:11], v[2:5], v[20:23], a[4:7]
	v_cvt_pk_f16_f32 v2, v144, v145
	v_cvt_pk_f16_f32 v3, v146, v147
	v_cvt_pk_f16_f32 v4, v148, v149
	v_cvt_pk_f16_f32 v5, v150, v151
	v_cvt_pk_f16_f32 v20, v95, v97
	s_waitcnt vmcnt(4)
	v_cvt_pk_f16_f32 v9, v106, v18
	v_cvt_pk_f16_f32 v21, v99, v101
	v_cvt_pk_f16_f32 v22, v103, v105
	s_waitcnt vmcnt(3)
	v_cvt_pk_f16_f32 v23, v107, v16
	v_mfma_f32_16x16x32_f16 a[4:7], v[2:5], v[6:9], a[0:3]
	global_store_dwordx4 v108, v[2:5], s[26:27] offset:192
	s_nop 0
	v_mfma_f32_16x16x32_f16 a[0:3], v[2:5], v[20:23], a[8:11]
	v_or_b32_e32 v18, 0x800, v14
	v_lshlrev_b64 v[16:17], 2, v[18:19]
	v_lshl_add_u64 v[20:21], s[4:5], 0, v[16:17]
	v_lshl_add_u64 v[16:17], s[10:11], 0, v[16:17]
	v_or_b32_e32 v18, 0x810, v14
	global_load_dword v46, v[16:17], off
	v_lshlrev_b64 v[16:17], 2, v[18:19]
	global_load_dword v37, v[20:21], off
	v_lshl_add_u64 v[20:21], s[4:5], 0, v[16:17]
	v_lshl_add_u64 v[16:17], s[10:11], 0, v[16:17]
	v_or_b32_e32 v18, 0x820, v14
	global_load_dword v48, v[16:17], off
	v_lshlrev_b64 v[16:17], 2, v[18:19]
	global_load_dword v47, v[20:21], off
	v_lshl_add_u64 v[20:21], s[4:5], 0, v[16:17]
	v_lshl_add_u64 v[16:17], s[10:11], 0, v[16:17]
	v_or_b32_e32 v18, 0x830, v14
	global_load_dword v50, v[16:17], off
	v_lshlrev_b64 v[16:17], 2, v[18:19]
	global_load_dword v49, v[20:21], off
	v_lshl_add_u64 v[20:21], s[4:5], 0, v[16:17]
	v_lshl_add_u64 v[16:17], s[10:11], 0, v[16:17]
	v_or_b32_e32 v18, 0x840, v14
	global_load_dword v52, v[16:17], off
	v_lshlrev_b64 v[16:17], 2, v[18:19]
	global_load_dword v51, v[20:21], off
	v_lshl_add_u64 v[20:21], s[4:5], 0, v[16:17]
	v_lshl_add_u64 v[16:17], s[10:11], 0, v[16:17]
	v_or_b32_e32 v18, 0x850, v14
	global_load_dword v54, v[16:17], off
	v_lshlrev_b64 v[16:17], 2, v[18:19]
	global_load_dword v53, v[20:21], off
	v_lshl_add_u64 v[20:21], s[4:5], 0, v[16:17]
	v_lshl_add_u64 v[16:17], s[10:11], 0, v[16:17]
	v_or_b32_e32 v18, 0x860, v14
	global_load_dword v56, v[16:17], off
	v_lshlrev_b64 v[16:17], 2, v[18:19]
	global_load_dword v55, v[20:21], off
	v_lshl_add_u64 v[20:21], s[4:5], 0, v[16:17]
	v_lshl_add_u64 v[16:17], s[10:11], 0, v[16:17]
	v_or_b32_e32 v18, 0x870, v14
	global_load_dword v58, v[16:17], off
	v_lshlrev_b64 v[16:17], 2, v[18:19]
	global_load_dword v57, v[20:21], off
	v_lshl_add_u64 v[20:21], s[4:5], 0, v[16:17]
	v_lshl_add_u64 v[16:17], s[10:11], 0, v[16:17]
	v_or_b32_e32 v18, 0xa00, v14
	global_load_dword v59, v[20:21], off
	global_load_dword v60, v[16:17], off
	s_nop 0
	v_lshlrev_b64 v[16:17], 2, v[18:19]
	v_lshl_add_u64 v[28:29], s[4:5], 0, v[16:17]
	v_lshl_add_u64 v[16:17], s[10:11], 0, v[16:17]
	v_or_b32_e32 v18, 0xa10, v14
	global_load_dword v62, v[16:17], off
	v_lshlrev_b64 v[16:17], 2, v[18:19]
	global_load_dword v61, v[28:29], off
	v_lshl_add_u64 v[28:29], s[4:5], 0, v[16:17]
	v_lshl_add_u64 v[16:17], s[10:11], 0, v[16:17]
	v_or_b32_e32 v18, 0xa20, v14
	global_load_dword v64, v[16:17], off
	v_lshlrev_b64 v[16:17], 2, v[18:19]
	global_load_dword v63, v[28:29], off
	v_lshl_add_u64 v[28:29], s[4:5], 0, v[16:17]
	v_lshl_add_u64 v[16:17], s[10:11], 0, v[16:17]
	v_or_b32_e32 v18, 0xa30, v14
	global_load_dword v66, v[16:17], off
	v_lshlrev_b64 v[16:17], 2, v[18:19]
	global_load_dword v65, v[28:29], off
	v_lshl_add_u64 v[28:29], s[4:5], 0, v[16:17]
	v_lshl_add_u64 v[16:17], s[10:11], 0, v[16:17]
	v_or_b32_e32 v18, 0xa40, v14
	global_load_dword v68, v[16:17], off
	v_lshlrev_b64 v[16:17], 2, v[18:19]
	global_load_dword v67, v[28:29], off
	v_lshl_add_u64 v[28:29], s[4:5], 0, v[16:17]
	v_lshl_add_u64 v[16:17], s[10:11], 0, v[16:17]
	v_or_b32_e32 v18, 0xa50, v14
	global_load_dword v70, v[16:17], off
	v_lshlrev_b64 v[16:17], 2, v[18:19]
	global_load_dword v69, v[28:29], off
	v_lshl_add_u64 v[28:29], s[4:5], 0, v[16:17]
	v_lshl_add_u64 v[16:17], s[10:11], 0, v[16:17]
	v_or_b32_e32 v18, 0xa60, v14
	global_load_dword v72, v[16:17], off
	v_lshlrev_b64 v[16:17], 2, v[18:19]
	global_load_dword v71, v[28:29], off
	v_lshl_add_u64 v[28:29], s[4:5], 0, v[16:17]
	v_lshl_add_u64 v[16:17], s[10:11], 0, v[16:17]
	v_or_b32_e32 v18, 0xa70, v14
	global_load_dword v74, v[16:17], off
	v_lshlrev_b64 v[16:17], 2, v[18:19]
	global_load_dword v73, v[28:29], off
	v_lshl_add_u64 v[28:29], s[4:5], 0, v[16:17]
	v_lshl_add_u64 v[16:17], s[10:11], 0, v[16:17]
	v_or_b32_e32 v18, 0xc00, v14
	global_load_dword v75, v[28:29], off
	global_load_dword v76, v[16:17], off
	s_nop 0
	v_lshlrev_b64 v[16:17], 2, v[18:19]
	v_lshl_add_u64 v[38:39], s[4:5], 0, v[16:17]
	v_lshl_add_u64 v[16:17], s[10:11], 0, v[16:17]
	v_or_b32_e32 v18, 0xc10, v14
	global_load_dword v78, v[16:17], off
	v_lshlrev_b64 v[16:17], 2, v[18:19]
	global_load_dword v77, v[38:39], off
	v_lshl_add_u64 v[38:39], s[4:5], 0, v[16:17]
	v_lshl_add_u64 v[16:17], s[10:11], 0, v[16:17]
	v_or_b32_e32 v18, 0xc20, v14
	global_load_dword v80, v[16:17], off
	v_lshlrev_b64 v[16:17], 2, v[18:19]
	global_load_dword v79, v[38:39], off
	v_lshl_add_u64 v[38:39], s[4:5], 0, v[16:17]
	v_lshl_add_u64 v[16:17], s[10:11], 0, v[16:17]
	v_or_b32_e32 v18, 0xc30, v14
	global_load_dword v82, v[16:17], off
	v_lshlrev_b64 v[16:17], 2, v[18:19]
	global_load_dword v81, v[38:39], off
	v_lshl_add_u64 v[38:39], s[4:5], 0, v[16:17]
	v_lshl_add_u64 v[16:17], s[10:11], 0, v[16:17]
	v_or_b32_e32 v18, 0xc40, v14
	global_load_dword v84, v[16:17], off
	v_lshlrev_b64 v[16:17], 2, v[18:19]
	global_load_dword v83, v[38:39], off
	v_lshl_add_u64 v[38:39], s[4:5], 0, v[16:17]
	v_lshl_add_u64 v[16:17], s[10:11], 0, v[16:17]
	v_or_b32_e32 v18, 0xc50, v14
	global_load_dword v86, v[16:17], off
	v_lshlrev_b64 v[16:17], 2, v[18:19]
	global_load_dword v85, v[38:39], off
	v_lshl_add_u64 v[38:39], s[4:5], 0, v[16:17]
	v_lshl_add_u64 v[16:17], s[10:11], 0, v[16:17]
	v_or_b32_e32 v18, 0xc60, v14
	global_load_dword v88, v[16:17], off
	v_lshlrev_b64 v[16:17], 2, v[18:19]
	global_load_dword v87, v[38:39], off
	v_lshl_add_u64 v[38:39], s[4:5], 0, v[16:17]
	v_lshl_add_u64 v[16:17], s[10:11], 0, v[16:17]
	v_or_b32_e32 v18, 0xc70, v14
	global_load_dword v90, v[16:17], off
	v_lshlrev_b64 v[16:17], 2, v[18:19]
	global_load_dword v89, v[38:39], off
	v_lshl_add_u64 v[38:39], s[4:5], 0, v[16:17]
	v_lshl_add_u64 v[16:17], s[10:11], 0, v[16:17]
	v_or_b32_e32 v18, 0xe00, v14
	global_load_dword v91, v[38:39], off
	global_load_dword v92, v[16:17], off
	s_nop 0
	v_lshlrev_b64 v[10:11], 2, v[18:19]
	v_lshl_add_u64 v[16:17], s[4:5], 0, v[10:11]
	v_lshl_add_u64 v[10:11], s[10:11], 0, v[10:11]
	v_or_b32_e32 v18, 0xe10, v14
	global_load_dword v94, v[10:11], off
	v_lshlrev_b64 v[10:11], 2, v[18:19]
	global_load_dword v93, v[16:17], off
	v_lshl_add_u64 v[16:17], s[4:5], 0, v[10:11]
	v_lshl_add_u64 v[10:11], s[10:11], 0, v[10:11]
	v_or_b32_e32 v18, 0xe20, v14
	global_load_dword v96, v[10:11], off
	v_lshlrev_b64 v[10:11], 2, v[18:19]
	global_load_dword v95, v[16:17], off
	v_lshl_add_u64 v[16:17], s[4:5], 0, v[10:11]
	v_lshl_add_u64 v[10:11], s[10:11], 0, v[10:11]
	v_or_b32_e32 v18, 0xe30, v14
	global_load_dword v98, v[10:11], off
	v_lshlrev_b64 v[10:11], 2, v[18:19]
	global_load_dword v97, v[16:17], off
	v_lshl_add_u64 v[16:17], s[4:5], 0, v[10:11]
	v_lshl_add_u64 v[10:11], s[10:11], 0, v[10:11]
	v_or_b32_e32 v18, 0xe40, v14
	global_load_dword v100, v[10:11], off
	v_lshlrev_b64 v[10:11], 2, v[18:19]
	global_load_dword v99, v[16:17], off
	v_lshl_add_u64 v[16:17], s[4:5], 0, v[10:11]
	v_lshl_add_u64 v[10:11], s[10:11], 0, v[10:11]
	v_or_b32_e32 v18, 0xe50, v14
	global_load_dword v102, v[10:11], off
	v_lshlrev_b64 v[10:11], 2, v[18:19]
	global_load_dword v101, v[16:17], off
	v_lshl_add_u64 v[16:17], s[4:5], 0, v[10:11]
	v_lshl_add_u64 v[10:11], s[10:11], 0, v[10:11]
	v_or_b32_e32 v18, 0xe60, v14
	global_load_dword v104, v[10:11], off
	v_lshlrev_b64 v[10:11], 2, v[18:19]
	global_load_dword v103, v[16:17], off
	v_lshl_add_u64 v[16:17], s[4:5], 0, v[10:11]
	v_lshl_add_u64 v[10:11], s[10:11], 0, v[10:11]
	v_or_b32_e32 v18, 0xe70, v14
	global_load_dword v106, v[10:11], off
	v_lshlrev_b64 v[10:11], 2, v[18:19]
	v_lshl_add_u64 v[14:15], s[4:5], 0, v[10:11]
	v_lshl_add_u64 v[10:11], s[10:11], 0, v[10:11]
	global_load_dword v105, v[16:17], off
	global_load_dword v18, v[14:15], off
	s_nop 0
	global_load_dword v10, v[10:11], off
	s_waitcnt lgkmcnt(0)
	v_lshlrev_b32_e32 v152, 2, v0
	s_add_u32 s28, s6, 0x1000
	s_addc_u32 s29, s7, 0
	s_add_u32 s30, s6, 0x2000
	s_addc_u32 s31, s7, 0
	s_add_u32 s32, s6, 0x3000
	s_addc_u32 s33, s7, 0
	s_add_u32 s34, s16, 0x1000
	s_addc_u32 s35, s17, 0
	s_add_u32 s36, s16, 0x2000
	s_addc_u32 s37, s17, 0
	s_add_u32 s38, s16, 0x3000
	s_addc_u32 s39, s17, 0
	global_load_dword v26, v152, s[6:7] offset:2048
	global_load_dword v27, v152, s[6:7] offset:3072
	global_load_dword v28, v152, s[28:29]
	global_load_dword v29, v152, s[28:29] offset:1024
	global_load_dword v38, v152, s[28:29] offset:2048
	global_load_dword v44, v152, s[28:29] offset:3072
	global_load_dword v39, v152, s[34:35]
	global_load_dword v41, v152, s[6:7]
	global_load_dword v109, v152, s[16:17]
	global_load_dword v110, v152, s[6:7] offset:1024
	global_load_dword v111, v152, s[16:17] offset:1024
	global_load_dword v144, v152, s[16:17] offset:2048
	global_load_dword v42, v152, s[8:9]
	global_load_dword v145, v152, s[16:17] offset:3072
	global_load_dword v40, v152, s[18:19]
	global_load_dword v146, v152, s[34:35] offset:1024
	global_load_dword v147, v152, s[34:35] offset:2048
	global_load_dword v148, v152, s[34:35] offset:3072
	global_load_dword v149, v152, s[30:31]
	global_load_dword v43, v152, s[30:31] offset:1024
	global_load_dword v30, v152, s[30:31] offset:2048
	global_load_dword v31, v152, s[30:31] offset:3072
	global_load_dword v45, v152, s[36:37]
	global_load_dword v150, v152, s[36:37] offset:1024
	global_load_dword v34, v152, s[36:37] offset:2048
	global_load_dword v35, v152, s[36:37] offset:3072
	global_load_dword v32, v152, s[32:33]
	global_load_dword v33, v152, s[32:33] offset:1024
	global_load_dword v151, v152, s[32:33] offset:2048
	global_load_dword v153, v152, s[32:33] offset:3072
	global_load_dword v154, v152, s[38:39]
	global_load_dword v155, v152, s[38:39] offset:1024
	global_load_dword v24, v152, s[38:39] offset:2048
	global_load_dword v25, v152, s[38:39] offset:3072
	s_waitcnt vmcnt(63)
	v_cvt_pk_f16_f32 v6, v112, v113
	v_cvt_pk_f16_f32 v7, v114, v115
	v_cvt_pk_f16_f32 v8, v116, v117
	v_cvt_pk_f16_f32 v9, v118, v119
	v_cvt_pk_f16_f32 v2, v37, v47
	v_cvt_pk_f16_f32 v3, v49, v51
	s_waitcnt vmcnt(63)
	v_cvt_pk_f16_f32 v4, v53, v55
	s_waitcnt vmcnt(63)
	v_cvt_pk_f16_f32 v5, v57, v59
	s_waitcnt vmcnt(63)
	v_cvt_pk_f16_f32 v14, v62, v64
	s_waitcnt vmcnt(63)
	v_cvt_pk_f16_f32 v15, v66, v68
	v_mfma_f32_16x16x32_f16 a[4:7], v[6:9], v[2:5], a[4:7]
	global_store_dwordx4 v108, v[6:9], s[26:27] offset:256
	v_cvt_pk_f16_f32 v2, v46, v48
	v_cvt_pk_f16_f32 v3, v50, v52
	v_cvt_pk_f16_f32 v4, v54, v56
	v_cvt_pk_f16_f32 v5, v58, v60
	s_waitcnt vmcnt(63)
	v_cvt_pk_f16_f32 v16, v70, v72
	s_waitcnt vmcnt(63)
	v_cvt_pk_f16_f32 v17, v74, v76
	v_mfma_f32_16x16x32_f16 a[0:3], v[6:9], v[2:5], a[0:3]
	v_cvt_pk_f16_f32 v2, v120, v121
	v_cvt_pk_f16_f32 v3, v122, v123
	v_cvt_pk_f16_f32 v4, v124, v125
	v_cvt_pk_f16_f32 v5, v126, v127
	v_cvt_pk_f16_f32 v6, v61, v63
	v_cvt_pk_f16_f32 v7, v65, v67
	v_cvt_pk_f16_f32 v8, v69, v71
	v_cvt_pk_f16_f32 v9, v73, v75
	v_mfma_f32_16x16x32_f16 a[0:3], v[2:5], v[14:17], a[0:3]
	global_store_dwordx4 v108, v[2:5], s[26:27] offset:320
	s_waitcnt vmcnt(63)
	v_cvt_pk_f16_f32 v14, v78, v80
	s_waitcnt vmcnt(61)
	v_cvt_pk_f16_f32 v15, v82, v84
	s_waitcnt vmcnt(57)
	v_cvt_pk_f16_f32 v16, v86, v88
	v_mfma_f32_16x16x32_f16 a[4:7], v[2:5], v[6:9], a[4:7]
	v_cvt_pk_f16_f32 v2, v128, v129
	v_cvt_pk_f16_f32 v3, v130, v131
	v_cvt_pk_f16_f32 v4, v132, v133
	v_cvt_pk_f16_f32 v5, v134, v135
	v_cvt_pk_f16_f32 v6, v77, v79
	v_cvt_pk_f16_f32 v7, v81, v83
	s_waitcnt vmcnt(56)
	v_cvt_pk_f16_f32 v8, v85, v87
	s_waitcnt vmcnt(53)
	v_cvt_pk_f16_f32 v9, v89, v91
	s_waitcnt vmcnt(52)
	v_cvt_pk_f16_f32 v17, v90, v92
	v_mfma_f32_16x16x32_f16 a[4:7], v[2:5], v[6:9], a[4:7]
	global_store_dwordx4 v108, v[2:5], s[26:27] offset:384
	s_waitcnt vmcnt(49)
	v_cvt_pk_f16_f32 v6, v93, v95
	s_waitcnt vmcnt(45)
	v_cvt_pk_f16_f32 v7, v97, v99
	s_waitcnt vmcnt(41)
	v_cvt_pk_f16_f32 v8, v101, v103
	v_mfma_f32_16x16x32_f16 a[0:3], v[2:5], v[14:17], a[0:3]
	v_cvt_pk_f16_f32 v2, v136, v137
	v_cvt_pk_f16_f32 v3, v138, v139
	v_cvt_pk_f16_f32 v4, v140, v141
	v_cvt_pk_f16_f32 v5, v142, v143
	v_cvt_pk_f16_f32 v14, v94, v96
	s_waitcnt vmcnt(38)
	v_cvt_pk_f16_f32 v9, v105, v18
	v_cvt_pk_f16_f32 v15, v98, v100
	v_cvt_pk_f16_f32 v16, v102, v104
	s_waitcnt vmcnt(37)
	v_cvt_pk_f16_f32 v17, v106, v10
	v_mfma_f32_16x16x32_f16 a[4:7], v[2:5], v[6:9], a[4:7]
	global_store_dwordx4 v108, v[2:5], s[26:27] offset:448
	s_nop 0
	v_mfma_f32_16x16x32_f16 a[0:3], v[2:5], v[14:17], a[0:3]
	v_lshlrev_b32_e32 v2, 11, v1
	v_lshlrev_b32_e32 v3, 2, v12
	v_lshlrev_b32_e32 v4, 8, v13
	v_lshlrev_b32_e32 v18, 2, v0
	s_movk_i32 s4, 0x3c0
	v_or3_b32 v2, v2, v3, v4
	v_and_or_b32 v10, v18, s4, v3
	ds_write_b32 v2, a4
	ds_write_b32 v2, a0 offset:1024
	ds_write_b32 v2, a5 offset:64
	ds_write_b32 v2, a1 offset:1088
	ds_write_b32 v2, a6 offset:128
	ds_write_b32 v2, a2 offset:1152
	ds_write_b32 v2, a7 offset:192
	ds_write_b32 v2, a3 offset:1216
	s_waitcnt lgkmcnt(0)
	s_barrier
	ds_read2st64_b32 v[2:3], v10 offset1:4
	ds_read2st64_b32 v[4:5], v10 offset0:8 offset1:12
	ds_read2st64_b32 v[6:7], v10 offset0:16 offset1:20
	ds_read2st64_b32 v[8:9], v10 offset0:24 offset1:28
	s_movk_i32 s4, 0x1000
	v_or_b32_e32 v20, 0x2000, v18
	s_waitcnt lgkmcnt(2)
	v_add_f32_e32 v2, v2, v4
	v_add_f32_e32 v3, v3, v5
	s_waitcnt lgkmcnt(1)
	v_add_f32_e32 v2, v2, v6
	v_add_f32_e32 v3, v3, v7
	v_lshl_add_u64 v[6:7], s[6:7], 0, v[18:19]
	s_waitcnt lgkmcnt(0)
	v_add_f32_e32 v2, v2, v8
	v_add_f32_e32 v3, v3, v9
	v_add_co_u32_e32 v4, vcc, s4, v6
	ds_write2st64_b32 v10, v2, v3 offset0:32 offset1:36
	v_or_b32_e32 v10, 0x1000, v18
	v_addc_co_u32_e32 v5, vcc, 0, v7, vcc
	s_waitcnt lgkmcnt(0)
	s_barrier
	s_waitcnt vmcnt(0)
	v_mov_b32_e32 v2, v26
	v_mov_b32_e32 v3, v27
	v_mov_b32_e32 v57, v28
	v_mov_b32_e32 v49, v29
	v_mov_b32_e32 v50, v38
	v_mov_b32_e32 v51, v39
	v_mov_b32_e32 v13, v41
	s_nop 0
	v_mov_b32_e32 v5, v109
	v_mov_b32_e32 v10, v110
	v_mov_b32_e32 v11, v111
	v_mov_b32_e32 v4, v144
	v_mov_b32_e32 v12, v145
	v_lshl_add_u64 v[8:9], s[16:17], 0, v[18:19]
	v_add_co_u32_e32 v14, vcc, s4, v8
	s_movk_i32 s4, 0x2000
	s_nop 0
	v_addc_co_u32_e32 v15, vcc, 0, v9, vcc
	v_add_co_u32_e32 v16, vcc, s4, v6
	s_mov_b32 s5, 0xc2000000
	s_nop 0
	v_addc_co_u32_e32 v17, vcc, 0, v7, vcc
	v_mov_b32_e32 v56, v146
	v_mov_b32_e32 v54, v147
	v_mov_b32_e32 v52, v148
	v_mov_b32_e32 v53, v149
	v_add_co_u32_e32 v14, vcc, s4, v8
	s_movk_i32 s4, 0x3000
	s_nop 0
	v_addc_co_u32_e32 v15, vcc, 0, v9, vcc
	v_add_co_u32_e32 v6, vcc, s4, v6
	v_or_b32_e32 v16, 0x3000, v18
	s_nop 0
	v_addc_co_u32_e32 v7, vcc, 0, v7, vcc
	v_mov_b32_e32 v46, v150
	v_mov_b32_e32 v20, v151
	v_mov_b32_e32 v21, v153
	v_mov_b32_e32 v22, v154
	v_add_co_u32_e32 v6, vcc, s4, v8
	s_and_b32 s4, s2, 0xffffff80
	s_nop 0
	v_addc_co_u32_e32 v7, vcc, 0, v9, vcc
	v_mov_b32_e32 v23, v155
	v_lshl_or_b32 v6, v1, 5, s4
	s_lshr_b32 s4, s2, 2
	v_and_or_b32 v70, s4, 31, v6
	ds_read_b128 v[6:9], v19 offset:8192
	ds_read_b128 v[14:17], v19 offset:9216
	ds_read_b128 v[26:29], v19 offset:8208
	ds_read_b128 v[58:61], v19 offset:8224
	ds_read_b128 v[62:65], v19 offset:8240
	v_lshlrev_b32_e32 v18, 1, v36
	ds_read_b128 v[66:69], v19 offset:9232
	v_lshl_add_u64 v[72:73], s[24:25], 0, v[18:19]
	v_mov_b32_e32 v38, 0x42000000
	v_ashrrev_i32_e32 v71, 31, v70
	s_and_b32 s4, s22, 48
	s_lshl_b32 s22, s4, 7
	s_lshl_b32 s4, s4, 1
	s_waitcnt vmcnt(21) lgkmcnt(5)
	v_fma_f32 v18, v13, v6, v42
	v_fmac_f32_e32 v18, v10, v7
	s_waitcnt vmcnt(19) lgkmcnt(4)
	v_fma_f32 v37, v5, v14, v40
	v_fmac_f32_e32 v37, v11, v15
	v_fmac_f32_e32 v18, v2, v8
	v_fmac_f32_e32 v37, v4, v16
	v_fmac_f32_e32 v18, v3, v9
	v_fmac_f32_e32 v37, v12, v17
	ds_read_b128 v[6:9], v19 offset:9248
	s_waitcnt lgkmcnt(4)
	v_fmac_f32_e32 v18, v57, v26
	s_waitcnt lgkmcnt(1)
	v_fmac_f32_e32 v37, v51, v66
	v_fmac_f32_e32 v18, v49, v27
	s_waitcnt vmcnt(18)
	v_fmac_f32_e32 v37, v56, v67
	v_fmac_f32_e32 v18, v50, v28
	s_waitcnt vmcnt(17)
	v_fmac_f32_e32 v37, v54, v68
	v_fmac_f32_e32 v18, v44, v29
	s_waitcnt vmcnt(16)
	v_fmac_f32_e32 v37, v52, v69
	s_waitcnt vmcnt(15)
	v_fmac_f32_e32 v18, v53, v58
	s_waitcnt vmcnt(11) lgkmcnt(0)
	v_fmac_f32_e32 v37, v45, v6
	v_fmac_f32_e32 v18, v43, v59
	s_waitcnt vmcnt(10)
	v_fmac_f32_e32 v37, v46, v7
	v_pk_mul_f32 v[6:7], v[30:31], v[60:61]
	ds_read_b128 v[14:17], v19 offset:9264
	v_add_f32_e32 v6, v18, v6
	v_add_f32_e32 v18, v6, v7
	s_waitcnt vmcnt(8)
	v_pk_mul_f32 v[6:7], v[34:35], v[8:9]
	v_lshlrev_b64 v[26:27], 13, v[70:71]
	v_add_f32_e32 v6, v37, v6
	v_add_f32_e32 v8, v6, v7
	s_waitcnt vmcnt(6)
	v_pk_mul_f32 v[6:7], v[32:33], v[62:63]
	s_nop 0
	v_add_f32_e32 v6, v18, v6
	v_add_f32_e32 v9, v6, v7
	s_waitcnt vmcnt(2) lgkmcnt(0)
	v_pk_mul_f32 v[6:7], v[22:23], v[14:15]
	s_nop 0
	v_add_f32_e32 v6, v8, v6
	v_add_f32_e32 v8, v6, v7
	v_pk_mul_f32 v[6:7], v[20:21], v[64:65]
	s_nop 0
	v_add_f32_e32 v6, v9, v6
	v_add_f32_e32 v9, v6, v7
	s_waitcnt vmcnt(0)
	v_pk_mul_f32 v[6:7], v[24:25], v[16:17]
	s_nop 0
	v_add_f32_e32 v6, v8, v6
	v_add_f32_e32 v6, v6, v7
	v_med3_f32 v6, v6, s5, v38
	v_mul_f32_e32 v6, 0x3fb8aa3b, v6
	v_exp_f32_e32 v18, v6
	v_med3_f32 v6, v9, s5, v38
	v_mul_f32_e32 v6, 0x3fb8aa3b, v6
	v_exp_f32_e32 v37, v6
	v_lshl_add_u64 v[6:7], v[72:73], 0, v[26:27]
	v_cvt_pk_bf16_f32 v8, v18, s0
	v_lshl_add_u64 v[28:29], v[6:7], 0, s[22:23]
	global_store_short v[28:29], v8, off
	ds_read_b128 v[6:9], v19 offset:8256
	ds_read_b128 v[14:17], v19 offset:9280
	ds_read_b128 v[58:61], v19 offset:8272
	ds_read_b128 v[62:65], v19 offset:8288
	ds_read_b128 v[66:69], v19 offset:8304
	ds_read_b128 v[70:73], v19 offset:9296
	s_waitcnt lgkmcnt(5)
	v_fma_f32 v39, v13, v6, v42
	s_waitcnt lgkmcnt(4)
	v_fma_f32 v41, v5, v14, v40
	v_fmac_f32_e32 v39, v10, v7
	v_fmac_f32_e32 v41, v11, v15
	v_fmac_f32_e32 v39, v2, v8
	v_fmac_f32_e32 v41, v4, v16
	v_fmac_f32_e32 v39, v3, v9
	v_fmac_f32_e32 v41, v12, v17
	ds_read_b128 v[6:9], v19 offset:9312
	s_waitcnt lgkmcnt(4)
	v_fmac_f32_e32 v39, v57, v58
	s_waitcnt lgkmcnt(1)
	v_fmac_f32_e32 v41, v51, v70
	v_fmac_f32_e32 v39, v49, v59
	v_fmac_f32_e32 v41, v56, v71
	v_fmac_f32_e32 v39, v50, v60
	v_fmac_f32_e32 v41, v54, v72
	v_fmac_f32_e32 v39, v44, v61
	v_fmac_f32_e32 v41, v52, v73
	v_fmac_f32_e32 v39, v53, v62
	s_waitcnt lgkmcnt(0)
	v_fmac_f32_e32 v41, v45, v6
	v_fmac_f32_e32 v39, v43, v63
	v_fmac_f32_e32 v41, v46, v7
	v_pk_mul_f32 v[6:7], v[30:31], v[64:65]
	ds_read_b128 v[14:17], v19 offset:9328
	v_add_f32_e32 v6, v39, v6
	v_add_f32_e32 v39, v6, v7
	v_pk_mul_f32 v[6:7], v[34:35], v[8:9]
	s_nop 0
	v_add_f32_e32 v6, v41, v6
	v_add_f32_e32 v8, v6, v7
	v_pk_mul_f32 v[6:7], v[32:33], v[66:67]
	s_nop 0
	v_add_f32_e32 v6, v39, v6
	v_add_f32_e32 v9, v6, v7
	s_waitcnt lgkmcnt(0)
	v_pk_mul_f32 v[6:7], v[22:23], v[14:15]
	s_nop 0
	v_add_f32_e32 v6, v8, v6
	v_add_f32_e32 v8, v6, v7
	v_pk_mul_f32 v[6:7], v[20:21], v[68:69]
	s_nop 0
	v_add_f32_e32 v6, v9, v6
	v_add_f32_e32 v9, v6, v7
	v_pk_mul_f32 v[6:7], v[24:25], v[16:17]
	s_nop 0
	v_add_f32_e32 v6, v8, v6
	v_add_f32_e32 v6, v6, v7
	v_med3_f32 v6, v6, s5, v38
	v_mul_f32_e32 v6, 0x3fb8aa3b, v6
	v_med3_f32 v7, v9, s5, v38
	v_exp_f32_e32 v39, v6
	v_mul_f32_e32 v41, 0x3fb8aa3b, v7
	ds_read_b128 v[6:9], v19 offset:8320
	ds_read_b128 v[14:17], v19 offset:9344
	ds_read_b128 v[58:61], v19 offset:8336
	ds_read_b128 v[62:65], v19 offset:9360
	v_cvt_pk_bf16_f32 v47, v39, s0
	global_store_short v[28:29], v47, off offset:128
	s_waitcnt lgkmcnt(3)
	v_fma_f32 v47, v13, v6, v42
	s_waitcnt lgkmcnt(2)
	v_fma_f32 v48, v5, v14, v40
	v_fmac_f32_e32 v47, v10, v7
	v_fmac_f32_e32 v48, v11, v15
	v_fmac_f32_e32 v47, v2, v8
	v_fmac_f32_e32 v48, v4, v16
	v_fmac_f32_e32 v47, v3, v9
	v_fmac_f32_e32 v48, v12, v17
	s_waitcnt lgkmcnt(1)
	v_fmac_f32_e32 v47, v57, v58
	ds_read_b128 v[6:9], v19 offset:8352
	ds_read_b128 v[14:17], v19 offset:9376
	v_fmac_f32_e32 v47, v49, v59
	s_waitcnt lgkmcnt(2)
	v_fmac_f32_e32 v48, v51, v62
	v_fmac_f32_e32 v47, v50, v60
	v_fmac_f32_e32 v48, v56, v63
	v_fmac_f32_e32 v47, v44, v61
	v_fmac_f32_e32 v48, v54, v64
	ds_read_b128 v[58:61], v19 offset:8368
	s_waitcnt lgkmcnt(2)
	v_fmac_f32_e32 v47, v53, v6
	v_fmac_f32_e32 v48, v52, v65
	v_fmac_f32_e32 v47, v43, v7
	v_pk_mul_f32 v[6:7], v[30:31], v[8:9]
	ds_read_b128 v[62:65], v19 offset:9392
	s_waitcnt lgkmcnt(2)
	v_fmac_f32_e32 v48, v45, v14
	v_add_f32_e32 v6, v47, v6
	v_fmac_f32_e32 v48, v46, v15
	v_add_f32_e32 v8, v6, v7
	v_pk_mul_f32 v[6:7], v[34:35], v[16:17]
	v_exp_f32_e32 v41, v41
	v_add_f32_e32 v6, v48, v6
	v_add_f32_e32 v9, v6, v7
	s_waitcnt lgkmcnt(1)
	v_pk_mul_f32 v[6:7], v[32:33], v[58:59]
	s_nop 0
	v_add_f32_e32 v6, v8, v6
	v_add_f32_e32 v8, v6, v7
	s_waitcnt lgkmcnt(0)
	v_pk_mul_f32 v[6:7], v[22:23], v[62:63]
	s_nop 0
	v_add_f32_e32 v6, v9, v6
	v_add_f32_e32 v9, v6, v7
	v_pk_mul_f32 v[6:7], v[20:21], v[60:61]
	s_nop 0
	v_add_f32_e32 v6, v8, v6
	v_add_f32_e32 v8, v6, v7
	v_pk_mul_f32 v[6:7], v[24:25], v[64:65]
	s_nop 0
	v_add_f32_e32 v6, v9, v6
	v_add_f32_e32 v6, v6, v7
	v_med3_f32 v6, v6, s5, v38
	v_mul_f32_e32 v6, 0x3fb8aa3b, v6
	v_exp_f32_e32 v47, v6
	v_med3_f32 v6, v8, s5, v38
	v_mul_f32_e32 v6, 0x3fb8aa3b, v6
	v_exp_f32_e32 v48, v6
	v_cvt_pk_bf16_f32 v6, v47, s0
	global_store_short v[28:29], v6, off offset:256
	ds_read_b128 v[6:9], v19 offset:8384
	ds_read_b128 v[14:17], v19 offset:9408
	ds_read_b128 v[58:61], v19 offset:8400
	ds_read_b128 v[62:65], v19 offset:8416
	ds_read_b128 v[66:69], v19 offset:8432
	ds_read_b128 v[70:73], v19 offset:9424
	s_waitcnt lgkmcnt(5)
	v_fma_f32 v55, v13, v6, v42
	s_waitcnt lgkmcnt(4)
	v_fma_f32 v74, v5, v14, v40
	v_fmac_f32_e32 v55, v10, v7
	v_fmac_f32_e32 v74, v11, v15
	v_fmac_f32_e32 v55, v2, v8
	v_fmac_f32_e32 v74, v4, v16
	v_fmac_f32_e32 v55, v3, v9
	v_fmac_f32_e32 v74, v12, v17
	ds_read_b128 v[6:9], v19 offset:9440
	s_waitcnt lgkmcnt(4)
	v_fmac_f32_e32 v55, v57, v58
	s_waitcnt lgkmcnt(1)
	v_fmac_f32_e32 v74, v51, v70
	v_fmac_f32_e32 v55, v49, v59
	v_fmac_f32_e32 v74, v56, v71
	v_fmac_f32_e32 v55, v50, v60
	v_fmac_f32_e32 v74, v54, v72
	v_fmac_f32_e32 v55, v44, v61
	v_fmac_f32_e32 v74, v52, v73
	v_fmac_f32_e32 v55, v53, v62
	s_waitcnt lgkmcnt(0)
	v_fmac_f32_e32 v74, v45, v6
	v_fmac_f32_e32 v55, v43, v63
	v_fmac_f32_e32 v74, v46, v7
	v_pk_mul_f32 v[6:7], v[30:31], v[64:65]
	ds_read_b128 v[14:17], v19 offset:9456
	v_add_f32_e32 v6, v55, v6
	v_add_f32_e32 v55, v6, v7
	v_pk_mul_f32 v[6:7], v[34:35], v[8:9]
	s_nop 0
	v_add_f32_e32 v6, v74, v6
	v_add_f32_e32 v8, v6, v7
	v_pk_mul_f32 v[6:7], v[32:33], v[66:67]
	s_nop 0
	v_add_f32_e32 v6, v55, v6
	v_add_f32_e32 v9, v6, v7
	s_waitcnt lgkmcnt(0)
	v_pk_mul_f32 v[6:7], v[22:23], v[14:15]
	s_nop 0
	v_add_f32_e32 v6, v8, v6
	v_add_f32_e32 v8, v6, v7
	v_pk_mul_f32 v[6:7], v[20:21], v[68:69]
	s_nop 0
	v_add_f32_e32 v6, v9, v6
	v_add_f32_e32 v9, v6, v7
	v_pk_mul_f32 v[6:7], v[24:25], v[16:17]
	s_nop 0
	v_add_f32_e32 v6, v8, v6
	v_add_f32_e32 v6, v6, v7
	v_med3_f32 v6, v6, s5, v38
	v_mul_f32_e32 v6, 0x3fb8aa3b, v6
	v_med3_f32 v7, v9, s5, v38
	v_exp_f32_e32 v55, v6
	v_mul_f32_e32 v58, 0x3fb8aa3b, v7
	ds_read_b128 v[6:9], v19 offset:8448
	ds_read_b128 v[14:17], v19 offset:9472
	ds_read_b128 v[60:63], v19 offset:8464
	ds_read_b128 v[64:67], v19 offset:9488
	v_cvt_pk_bf16_f32 v59, v55, s0
	global_store_short v[28:29], v59, off offset:384
	s_waitcnt lgkmcnt(3)
	v_fma_f32 v59, v13, v6, v42
	s_waitcnt lgkmcnt(2)
	v_fma_f32 v68, v5, v14, v40
	v_fmac_f32_e32 v59, v10, v7
	v_fmac_f32_e32 v68, v11, v15
	v_fmac_f32_e32 v59, v2, v8
	v_fmac_f32_e32 v68, v4, v16
	v_fmac_f32_e32 v59, v3, v9
	v_fmac_f32_e32 v68, v12, v17
	s_waitcnt lgkmcnt(1)
	v_fmac_f32_e32 v59, v57, v60
	ds_read_b128 v[6:9], v19 offset:8480
	ds_read_b128 v[14:17], v19 offset:9504
	v_fmac_f32_e32 v59, v49, v61
	s_waitcnt lgkmcnt(2)
	v_fmac_f32_e32 v68, v51, v64
	v_fmac_f32_e32 v59, v50, v62
	v_fmac_f32_e32 v68, v56, v65
	v_fmac_f32_e32 v59, v44, v63
	v_fmac_f32_e32 v68, v54, v66
	ds_read_b128 v[60:63], v19 offset:8496
	s_waitcnt lgkmcnt(2)
	v_fmac_f32_e32 v59, v53, v6
	v_fmac_f32_e32 v68, v52, v67
	v_fmac_f32_e32 v59, v43, v7
	v_pk_mul_f32 v[6:7], v[30:31], v[8:9]
	ds_read_b128 v[64:67], v19 offset:9520
	s_waitcnt lgkmcnt(2)
	v_fmac_f32_e32 v68, v45, v14
	v_add_f32_e32 v6, v59, v6
	v_fmac_f32_e32 v68, v46, v15
	v_add_f32_e32 v8, v6, v7
	v_pk_mul_f32 v[6:7], v[34:35], v[16:17]
	v_exp_f32_e32 v58, v58
	v_add_f32_e32 v6, v68, v6
	v_add_f32_e32 v9, v6, v7
	s_waitcnt lgkmcnt(1)
	v_pk_mul_f32 v[6:7], v[32:33], v[60:61]
	s_nop 0
	v_add_f32_e32 v6, v8, v6
	v_add_f32_e32 v8, v6, v7
	s_waitcnt lgkmcnt(0)
	v_pk_mul_f32 v[6:7], v[22:23], v[64:65]
	s_nop 0
	v_add_f32_e32 v6, v9, v6
	v_add_f32_e32 v9, v6, v7
	v_pk_mul_f32 v[6:7], v[20:21], v[62:63]
	s_nop 0
	v_add_f32_e32 v6, v8, v6
	v_add_f32_e32 v8, v6, v7
	v_pk_mul_f32 v[6:7], v[24:25], v[66:67]
	s_nop 0
	v_add_f32_e32 v6, v9, v6
	v_add_f32_e32 v6, v6, v7
	v_med3_f32 v6, v6, s5, v38
	v_mul_f32_e32 v6, 0x3fb8aa3b, v6
	v_exp_f32_e32 v59, v6
	v_med3_f32 v6, v8, s5, v38
	v_mul_f32_e32 v6, 0x3fb8aa3b, v6
	v_exp_f32_e32 v60, v6
	v_cvt_pk_bf16_f32 v6, v59, s0
	global_store_short v[28:29], v6, off offset:512
	ds_read_b128 v[6:9], v19 offset:8512
	ds_read_b128 v[14:17], v19 offset:9536
	ds_read_b128 v[62:65], v19 offset:8528
	ds_read_b128 v[66:69], v19 offset:8544
	ds_read_b128 v[70:73], v19 offset:8560
	ds_read_b128 v[74:77], v19 offset:9552
	s_waitcnt lgkmcnt(5)
	v_fma_f32 v61, v13, v6, v42
	s_waitcnt lgkmcnt(4)
	v_fma_f32 v78, v5, v14, v40
	v_fmac_f32_e32 v61, v10, v7
	v_fmac_f32_e32 v78, v11, v15
	v_fmac_f32_e32 v61, v2, v8
	v_fmac_f32_e32 v78, v4, v16
	v_fmac_f32_e32 v61, v3, v9
	v_fmac_f32_e32 v78, v12, v17
	ds_read_b128 v[6:9], v19 offset:9568
	s_waitcnt lgkmcnt(4)
	v_fmac_f32_e32 v61, v57, v62
	s_waitcnt lgkmcnt(1)
	v_fmac_f32_e32 v78, v51, v74
	v_fmac_f32_e32 v61, v49, v63
	v_fmac_f32_e32 v78, v56, v75
	v_fmac_f32_e32 v61, v50, v64
	v_fmac_f32_e32 v78, v54, v76
	v_fmac_f32_e32 v61, v44, v65
	v_fmac_f32_e32 v78, v52, v77
	v_fmac_f32_e32 v61, v53, v66
	s_waitcnt lgkmcnt(0)
	v_fmac_f32_e32 v78, v45, v6
	v_fmac_f32_e32 v61, v43, v67
	v_fmac_f32_e32 v78, v46, v7
	v_pk_mul_f32 v[6:7], v[30:31], v[68:69]
	ds_read_b128 v[14:17], v19 offset:9584
	v_add_f32_e32 v6, v61, v6
	v_add_f32_e32 v61, v6, v7
	v_pk_mul_f32 v[6:7], v[34:35], v[8:9]
	s_nop 0
	v_add_f32_e32 v6, v78, v6
	v_add_f32_e32 v8, v6, v7
	v_pk_mul_f32 v[6:7], v[32:33], v[70:71]
	s_nop 0
	v_add_f32_e32 v6, v61, v6
	v_add_f32_e32 v9, v6, v7
	s_waitcnt lgkmcnt(0)
	v_pk_mul_f32 v[6:7], v[22:23], v[14:15]
	s_nop 0
	v_add_f32_e32 v6, v8, v6
	v_add_f32_e32 v8, v6, v7
	v_pk_mul_f32 v[6:7], v[20:21], v[72:73]
	s_nop 0
	v_add_f32_e32 v6, v9, v6
	v_add_f32_e32 v9, v6, v7
	v_pk_mul_f32 v[6:7], v[24:25], v[16:17]
	s_nop 0
	v_add_f32_e32 v6, v8, v6
	v_add_f32_e32 v6, v6, v7
	v_med3_f32 v6, v6, s5, v38
	v_mul_f32_e32 v6, 0x3fb8aa3b, v6
	v_med3_f32 v7, v9, s5, v38
	v_exp_f32_e32 v61, v6
	v_mul_f32_e32 v62, 0x3fb8aa3b, v7
	ds_read_b128 v[6:9], v19 offset:8576
	ds_read_b128 v[14:17], v19 offset:9600
	ds_read_b128 v[64:67], v19 offset:8592
	ds_read_b128 v[68:71], v19 offset:9616
	v_cvt_pk_bf16_f32 v63, v61, s0
	global_store_short v[28:29], v63, off offset:640
	s_waitcnt lgkmcnt(3)
	v_fma_f32 v63, v13, v6, v42
	s_waitcnt lgkmcnt(2)
	v_fma_f32 v72, v5, v14, v40
	v_fmac_f32_e32 v63, v10, v7
	v_fmac_f32_e32 v72, v11, v15
	v_fmac_f32_e32 v63, v2, v8
	v_fmac_f32_e32 v72, v4, v16
	v_fmac_f32_e32 v63, v3, v9
	v_fmac_f32_e32 v72, v12, v17
	s_waitcnt lgkmcnt(1)
	v_fmac_f32_e32 v63, v57, v64
	ds_read_b128 v[6:9], v19 offset:8608
	ds_read_b128 v[14:17], v19 offset:9632
	v_fmac_f32_e32 v63, v49, v65
	s_waitcnt lgkmcnt(2)
	v_fmac_f32_e32 v72, v51, v68
	v_fmac_f32_e32 v63, v50, v66
	v_fmac_f32_e32 v72, v56, v69
	v_fmac_f32_e32 v63, v44, v67
	v_fmac_f32_e32 v72, v54, v70
	ds_read_b128 v[64:67], v19 offset:8624
	s_waitcnt lgkmcnt(2)
	v_fmac_f32_e32 v63, v53, v6
	v_fmac_f32_e32 v72, v52, v71
	v_fmac_f32_e32 v63, v43, v7
	v_pk_mul_f32 v[6:7], v[30:31], v[8:9]
	ds_read_b128 v[68:71], v19 offset:9648
	s_waitcnt lgkmcnt(2)
	v_fmac_f32_e32 v72, v45, v14
	v_add_f32_e32 v6, v63, v6
	v_fmac_f32_e32 v72, v46, v15
	v_add_f32_e32 v8, v6, v7
	v_pk_mul_f32 v[6:7], v[34:35], v[16:17]
	v_exp_f32_e32 v62, v62
	v_add_f32_e32 v6, v72, v6
	v_add_f32_e32 v9, v6, v7
	s_waitcnt lgkmcnt(1)
	v_pk_mul_f32 v[6:7], v[32:33], v[64:65]
	s_nop 0
	v_add_f32_e32 v6, v8, v6
	v_add_f32_e32 v8, v6, v7
	s_waitcnt lgkmcnt(0)
	v_pk_mul_f32 v[6:7], v[22:23], v[68:69]
	s_nop 0
	v_add_f32_e32 v6, v9, v6
	v_add_f32_e32 v9, v6, v7
	v_pk_mul_f32 v[6:7], v[20:21], v[66:67]
	s_nop 0
	v_add_f32_e32 v6, v8, v6
	v_add_f32_e32 v8, v6, v7
	v_pk_mul_f32 v[6:7], v[24:25], v[70:71]
	s_nop 0
	v_add_f32_e32 v6, v9, v6
	v_add_f32_e32 v6, v6, v7
	v_med3_f32 v6, v6, s5, v38
	v_mul_f32_e32 v6, 0x3fb8aa3b, v6
	v_exp_f32_e32 v63, v6
	v_med3_f32 v6, v8, s5, v38
	v_mul_f32_e32 v6, 0x3fb8aa3b, v6
	v_exp_f32_e32 v64, v6
	v_cvt_pk_bf16_f32 v6, v63, s0
	global_store_short v[28:29], v6, off offset:768
	ds_read_b128 v[6:9], v19 offset:8640
	ds_read_b128 v[14:17], v19 offset:9664
	ds_read_b128 v[66:69], v19 offset:8656
	ds_read_b128 v[70:73], v19 offset:8672
	ds_read_b128 v[74:77], v19 offset:8688
	ds_read_b128 v[78:81], v19 offset:9680
	s_waitcnt lgkmcnt(5)
	v_fma_f32 v65, v13, v6, v42
	s_waitcnt lgkmcnt(4)
	v_fma_f32 v82, v5, v14, v40
	v_fmac_f32_e32 v65, v10, v7
	v_fmac_f32_e32 v82, v11, v15
	v_fmac_f32_e32 v65, v2, v8
	v_fmac_f32_e32 v82, v4, v16
	v_fmac_f32_e32 v65, v3, v9
	v_fmac_f32_e32 v82, v12, v17
	ds_read_b128 v[6:9], v19 offset:9696
	s_waitcnt lgkmcnt(4)
	v_fmac_f32_e32 v65, v57, v66
	s_waitcnt lgkmcnt(1)
	v_fmac_f32_e32 v82, v51, v78
	v_fmac_f32_e32 v65, v49, v67
	v_fmac_f32_e32 v82, v56, v79
	v_fmac_f32_e32 v65, v50, v68
	v_fmac_f32_e32 v82, v54, v80
	v_fmac_f32_e32 v65, v44, v69
	v_fmac_f32_e32 v82, v52, v81
	v_fmac_f32_e32 v65, v53, v70
	s_waitcnt lgkmcnt(0)
	v_fmac_f32_e32 v82, v45, v6
	v_fmac_f32_e32 v65, v43, v71
	v_fmac_f32_e32 v82, v46, v7
	v_pk_mul_f32 v[6:7], v[30:31], v[72:73]
	ds_read_b128 v[14:17], v19 offset:9712
	v_add_f32_e32 v6, v65, v6
	v_add_f32_e32 v65, v6, v7
	v_pk_mul_f32 v[6:7], v[34:35], v[8:9]
	s_nop 0
	v_add_f32_e32 v6, v82, v6
	v_add_f32_e32 v8, v6, v7
	v_pk_mul_f32 v[6:7], v[32:33], v[74:75]
	s_nop 0
	v_add_f32_e32 v6, v65, v6
	v_add_f32_e32 v9, v6, v7
	s_waitcnt lgkmcnt(0)
	v_pk_mul_f32 v[6:7], v[22:23], v[14:15]
	s_nop 0
	v_add_f32_e32 v6, v8, v6
	v_add_f32_e32 v8, v6, v7
	v_pk_mul_f32 v[6:7], v[20:21], v[76:77]
	s_nop 0
	v_add_f32_e32 v6, v9, v6
	v_add_f32_e32 v9, v6, v7
	v_pk_mul_f32 v[6:7], v[24:25], v[16:17]
	s_nop 0
	v_add_f32_e32 v6, v8, v6
	v_add_f32_e32 v6, v6, v7
	v_med3_f32 v6, v6, s5, v38
	v_mul_f32_e32 v6, 0x3fb8aa3b, v6
	v_exp_f32_e32 v65, v6
	v_med3_f32 v6, v9, s5, v38
	v_mul_f32_e32 v6, 0x3fb8aa3b, v6
	v_exp_f32_e32 v66, v6
	v_cvt_pk_bf16_f32 v6, v65, s0
	global_store_short v[28:29], v6, off offset:896
	ds_read_b128 v[6:9], v19 offset:8704
	ds_read_b128 v[14:17], v19 offset:9728
	ds_read_b128 v[68:71], v19 offset:8720
	ds_read_b128 v[72:75], v19 offset:8736
	ds_read_b128 v[76:79], v19 offset:8752
	ds_read_b128 v[80:83], v19 offset:9744
	s_waitcnt lgkmcnt(5)
	v_fma_f32 v67, v13, v6, v42
	s_waitcnt lgkmcnt(4)
	v_fma_f32 v84, v5, v14, v40
	v_fmac_f32_e32 v67, v10, v7
	v_fmac_f32_e32 v84, v11, v15
	v_fmac_f32_e32 v67, v2, v8
	v_fmac_f32_e32 v84, v4, v16
	v_fmac_f32_e32 v67, v3, v9
	v_fmac_f32_e32 v84, v12, v17
	ds_read_b128 v[6:9], v19 offset:9760
	s_waitcnt lgkmcnt(4)
	v_fmac_f32_e32 v67, v57, v68
	s_waitcnt lgkmcnt(1)
	v_fmac_f32_e32 v84, v51, v80
	v_fmac_f32_e32 v67, v49, v69
	v_fmac_f32_e32 v84, v56, v81
	v_fmac_f32_e32 v67, v50, v70
	v_fmac_f32_e32 v84, v54, v82
	v_fmac_f32_e32 v67, v44, v71
	v_fmac_f32_e32 v84, v52, v83
	v_fmac_f32_e32 v67, v53, v72
	s_waitcnt lgkmcnt(0)
	v_fmac_f32_e32 v84, v45, v6
	v_fmac_f32_e32 v67, v43, v73
	v_fmac_f32_e32 v84, v46, v7
	v_pk_mul_f32 v[6:7], v[30:31], v[74:75]
	ds_read_b128 v[14:17], v19 offset:9776
	v_add_f32_e32 v6, v67, v6
	v_add_f32_e32 v67, v6, v7
	v_pk_mul_f32 v[6:7], v[34:35], v[8:9]
	s_nop 0
	v_add_f32_e32 v6, v84, v6
	v_add_f32_e32 v8, v6, v7
	v_pk_mul_f32 v[6:7], v[32:33], v[76:77]
	s_nop 0
	v_add_f32_e32 v6, v67, v6
	v_add_f32_e32 v9, v6, v7
	s_waitcnt lgkmcnt(0)
	v_pk_mul_f32 v[6:7], v[22:23], v[14:15]
	s_nop 0
	v_add_f32_e32 v6, v8, v6
	v_add_f32_e32 v8, v6, v7
	v_pk_mul_f32 v[6:7], v[20:21], v[78:79]
	s_nop 0
	v_add_f32_e32 v6, v9, v6
	v_add_f32_e32 v9, v6, v7
	v_pk_mul_f32 v[6:7], v[24:25], v[16:17]
	s_nop 0
	v_add_f32_e32 v6, v8, v6
	v_add_f32_e32 v6, v6, v7
	v_med3_f32 v6, v6, s5, v38
	v_mul_f32_e32 v6, 0x3fb8aa3b, v6
	v_exp_f32_e32 v67, v6
	v_med3_f32 v6, v9, s5, v38
	v_mul_f32_e32 v6, 0x3fb8aa3b, v6
	v_exp_f32_e32 v68, v6
	v_cvt_pk_bf16_f32 v6, v67, s0
	global_store_short v[28:29], v6, off offset:1024
	ds_read_b128 v[6:9], v19 offset:8768
	ds_read_b128 v[14:17], v19 offset:9792
	ds_read_b128 v[70:73], v19 offset:8784
	ds_read_b128 v[74:77], v19 offset:8800
	ds_read_b128 v[78:81], v19 offset:8816
	ds_read_b128 v[82:85], v19 offset:9808
	s_waitcnt lgkmcnt(5)
	v_fma_f32 v69, v13, v6, v42
	s_waitcnt lgkmcnt(4)
	v_fma_f32 v86, v5, v14, v40
	v_fmac_f32_e32 v69, v10, v7
	v_fmac_f32_e32 v86, v11, v15
	v_fmac_f32_e32 v69, v2, v8
	v_fmac_f32_e32 v86, v4, v16
	v_fmac_f32_e32 v69, v3, v9
	v_fmac_f32_e32 v86, v12, v17
	ds_read_b128 v[6:9], v19 offset:9824
	s_waitcnt lgkmcnt(4)
	v_fmac_f32_e32 v69, v57, v70
	s_waitcnt lgkmcnt(1)
	v_fmac_f32_e32 v86, v51, v82
	v_fmac_f32_e32 v69, v49, v71
	v_fmac_f32_e32 v86, v56, v83
	v_fmac_f32_e32 v69, v50, v72
	v_fmac_f32_e32 v86, v54, v84
	v_fmac_f32_e32 v69, v44, v73
	v_fmac_f32_e32 v86, v52, v85
	v_fmac_f32_e32 v69, v53, v74
	s_waitcnt lgkmcnt(0)
	v_fmac_f32_e32 v86, v45, v6
	v_fmac_f32_e32 v69, v43, v75
	v_fmac_f32_e32 v86, v46, v7
	v_pk_mul_f32 v[6:7], v[30:31], v[76:77]
	ds_read_b128 v[14:17], v19 offset:9840
	v_add_f32_e32 v6, v69, v6
	v_add_f32_e32 v69, v6, v7
	v_pk_mul_f32 v[6:7], v[34:35], v[8:9]
	ds_read_b128 v[72:75], v19 offset:8848
	v_add_f32_e32 v6, v86, v6
	v_add_f32_e32 v8, v6, v7
	v_pk_mul_f32 v[6:7], v[32:33], v[78:79]
	ds_read_b128 v[76:79], v19 offset:9872
	v_add_f32_e32 v6, v69, v6
	v_add_f32_e32 v9, v6, v7
	s_waitcnt lgkmcnt(2)
	v_pk_mul_f32 v[6:7], v[22:23], v[14:15]
	s_nop 0
	v_add_f32_e32 v6, v8, v6
	v_add_f32_e32 v8, v6, v7
	v_pk_mul_f32 v[6:7], v[20:21], v[80:81]
	s_nop 0
	v_add_f32_e32 v6, v9, v6
	v_add_f32_e32 v9, v6, v7
	v_pk_mul_f32 v[6:7], v[24:25], v[16:17]
	ds_read_b128 v[14:17], v19 offset:9856
	v_add_f32_e32 v6, v8, v6
	v_add_f32_e32 v6, v6, v7
	v_med3_f32 v6, v6, s5, v38
	v_mul_f32_e32 v6, 0x3fb8aa3b, v6
	v_exp_f32_e32 v69, v6
	v_med3_f32 v6, v9, s5, v38
	v_mul_f32_e32 v6, 0x3fb8aa3b, v6
	v_exp_f32_e32 v70, v6
	ds_read_b128 v[6:9], v19 offset:8832
	v_cvt_pk_bf16_f32 v71, v69, s0
	global_store_short v[28:29], v71, off offset:1152
	s_waitcnt lgkmcnt(1)
	v_fma_f32 v80, v5, v14, v40
	v_fmac_f32_e32 v80, v11, v15
	s_waitcnt lgkmcnt(0)
	v_fma_f32 v71, v13, v6, v42
	v_fmac_f32_e32 v71, v10, v7
	v_fmac_f32_e32 v71, v2, v8
	v_fmac_f32_e32 v71, v3, v9
	v_fmac_f32_e32 v71, v57, v72
	v_fmac_f32_e32 v80, v4, v16
	v_fmac_f32_e32 v71, v49, v73
	v_fmac_f32_e32 v80, v12, v17
	ds_read_b128 v[6:9], v19 offset:8864
	ds_read_b128 v[14:17], v19 offset:8880
	v_fmac_f32_e32 v71, v50, v74
	v_fmac_f32_e32 v71, v44, v75
	ds_read_b128 v[72:75], v19 offset:9888
	v_fmac_f32_e32 v80, v51, v76
	v_fmac_f32_e32 v80, v56, v77
	v_fmac_f32_e32 v80, v54, v78
	s_waitcnt lgkmcnt(2)
	v_fmac_f32_e32 v71, v53, v6
	v_fmac_f32_e32 v80, v52, v79
	v_fmac_f32_e32 v71, v43, v7
	v_pk_mul_f32 v[6:7], v[30:31], v[8:9]
	ds_read_b128 v[76:79], v19 offset:9904
	s_waitcnt lgkmcnt(1)
	v_fmac_f32_e32 v80, v45, v72
	v_add_f32_e32 v6, v71, v6
	v_fmac_f32_e32 v80, v46, v73
	v_add_f32_e32 v8, v6, v7
	v_pk_mul_f32 v[6:7], v[34:35], v[74:75]
	s_nop 0
	v_add_f32_e32 v6, v80, v6
	v_add_f32_e32 v9, v6, v7
	v_pk_mul_f32 v[6:7], v[32:33], v[14:15]
	s_nop 0
	v_add_f32_e32 v6, v8, v6
	v_add_f32_e32 v8, v6, v7
	s_waitcnt lgkmcnt(0)
	v_pk_mul_f32 v[6:7], v[22:23], v[76:77]
	ds_read_b128 v[74:77], v19 offset:8912
	v_add_f32_e32 v6, v9, v6
	v_add_f32_e32 v9, v6, v7
	v_pk_mul_f32 v[6:7], v[20:21], v[16:17]
	ds_read_b128 v[14:17], v19 offset:9920
	v_add_f32_e32 v6, v8, v6
	v_add_f32_e32 v8, v6, v7
	v_pk_mul_f32 v[6:7], v[24:25], v[78:79]
	ds_read_b128 v[78:81], v19 offset:9936
	v_add_f32_e32 v6, v9, v6
	v_add_f32_e32 v6, v6, v7
	v_med3_f32 v6, v6, s5, v38
	v_mul_f32_e32 v6, 0x3fb8aa3b, v6
	v_exp_f32_e32 v71, v6
	v_med3_f32 v6, v8, s5, v38
	v_mul_f32_e32 v6, 0x3fb8aa3b, v6
	v_exp_f32_e32 v72, v6
	ds_read_b128 v[6:9], v19 offset:8896
	v_cvt_pk_bf16_f32 v73, v71, s0
	global_store_short v[28:29], v73, off offset:1280
	s_waitcnt lgkmcnt(2)
	v_fma_f32 v82, v5, v14, v40
	v_fmac_f32_e32 v82, v11, v15
	s_waitcnt lgkmcnt(0)
	v_fma_f32 v73, v13, v6, v42
	v_fmac_f32_e32 v73, v10, v7
	v_fmac_f32_e32 v73, v2, v8
	v_fmac_f32_e32 v73, v3, v9
	v_fmac_f32_e32 v73, v57, v74
	v_fmac_f32_e32 v82, v4, v16
	v_fmac_f32_e32 v73, v49, v75
	v_fmac_f32_e32 v82, v12, v17
	ds_read_b128 v[6:9], v19 offset:8928
	ds_read_b128 v[14:17], v19 offset:8944
	v_fmac_f32_e32 v73, v50, v76
	v_fmac_f32_e32 v73, v44, v77
	ds_read_b128 v[74:77], v19 offset:9952
	v_fmac_f32_e32 v82, v51, v78
	v_fmac_f32_e32 v82, v56, v79
	v_fmac_f32_e32 v82, v54, v80
	s_waitcnt lgkmcnt(2)
	v_fmac_f32_e32 v73, v53, v6
	v_fmac_f32_e32 v82, v52, v81
	v_fmac_f32_e32 v73, v43, v7
	v_pk_mul_f32 v[6:7], v[30:31], v[8:9]
	ds_read_b128 v[78:81], v19 offset:9968
	s_waitcnt lgkmcnt(1)
	v_fmac_f32_e32 v82, v45, v74
	v_add_f32_e32 v6, v73, v6
	v_fmac_f32_e32 v82, v46, v75
	v_add_f32_e32 v8, v6, v7
	v_pk_mul_f32 v[6:7], v[34:35], v[76:77]
	s_nop 0
	v_add_f32_e32 v6, v82, v6
	v_add_f32_e32 v9, v6, v7
	v_pk_mul_f32 v[6:7], v[32:33], v[14:15]
	s_nop 0
	v_add_f32_e32 v6, v8, v6
	v_add_f32_e32 v8, v6, v7
	s_waitcnt lgkmcnt(0)
	v_pk_mul_f32 v[6:7], v[22:23], v[78:79]
	s_nop 0
	v_add_f32_e32 v6, v9, v6
	v_add_f32_e32 v9, v6, v7
	v_pk_mul_f32 v[6:7], v[20:21], v[16:17]
	s_nop 0
	v_add_f32_e32 v6, v8, v6
	v_add_f32_e32 v8, v6, v7
	v_pk_mul_f32 v[6:7], v[24:25], v[80:81]
	s_nop 0
	v_add_f32_e32 v6, v9, v6
	v_add_f32_e32 v6, v6, v7
	v_med3_f32 v6, v6, s5, v38
	v_med3_f32 v7, v8, s5, v38
	v_mul_f32_e32 v6, 0x3fb8aa3b, v6
	v_mul_f32_e32 v7, 0x3fb8aa3b, v7
	v_exp_f32_e32 v73, v6
	v_exp_f32_e32 v74, v7
	ds_read_b128 v[6:9], v19 offset:8960
	ds_read_b128 v[14:17], v19 offset:9984
	ds_read_b128 v[76:79], v19 offset:8976
	v_cvt_pk_bf16_f32 v75, v73, s0
	global_store_short v[28:29], v75, off offset:1408
	s_waitcnt lgkmcnt(2)
	v_fma_f32 v75, v13, v6, v42
	v_fmac_f32_e32 v75, v10, v7
	ds_read_b128 v[80:83], v19 offset:10000
	v_fmac_f32_e32 v75, v2, v8
	s_waitcnt lgkmcnt(2)
	v_fma_f32 v84, v5, v14, v40
	v_fmac_f32_e32 v75, v3, v9
	v_fmac_f32_e32 v84, v11, v15
	ds_read_b128 v[6:9], v19 offset:8992
	s_waitcnt lgkmcnt(2)
	v_fmac_f32_e32 v75, v57, v76
	v_fmac_f32_e32 v84, v4, v16
	v_fmac_f32_e32 v75, v49, v77
	v_fmac_f32_e32 v84, v12, v17
	v_fmac_f32_e32 v75, v50, v78
	ds_read_b128 v[14:17], v19 offset:10016
	v_fmac_f32_e32 v75, v44, v79
	ds_read_b128 v[76:79], v19 offset:9008
	s_waitcnt lgkmcnt(3)
	v_fmac_f32_e32 v84, v51, v80
	v_fmac_f32_e32 v84, v56, v81
	v_fmac_f32_e32 v84, v54, v82
	s_waitcnt lgkmcnt(2)
	v_fmac_f32_e32 v75, v53, v6
	v_fmac_f32_e32 v84, v52, v83
	v_fmac_f32_e32 v75, v43, v7
	v_pk_mul_f32 v[6:7], v[30:31], v[8:9]
	ds_read_b128 v[80:83], v19 offset:10032
	s_waitcnt lgkmcnt(2)
	v_fmac_f32_e32 v84, v45, v14
	v_add_f32_e32 v6, v75, v6
	v_fmac_f32_e32 v84, v46, v15
	v_add_f32_e32 v8, v6, v7
	v_pk_mul_f32 v[6:7], v[34:35], v[16:17]
	s_nop 0
	v_add_f32_e32 v6, v84, v6
	v_add_f32_e32 v9, v6, v7
	s_waitcnt lgkmcnt(1)
	v_pk_mul_f32 v[6:7], v[32:33], v[76:77]
	s_nop 0
	v_add_f32_e32 v6, v8, v6
	v_add_f32_e32 v8, v6, v7
	s_waitcnt lgkmcnt(0)
	v_pk_mul_f32 v[6:7], v[22:23], v[80:81]
	s_nop 0
	v_add_f32_e32 v6, v9, v6
	v_add_f32_e32 v9, v6, v7
	v_pk_mul_f32 v[6:7], v[20:21], v[78:79]
	s_nop 0
	v_add_f32_e32 v6, v8, v6
	v_add_f32_e32 v8, v6, v7
	v_pk_mul_f32 v[6:7], v[24:25], v[82:83]
	s_nop 0
	v_add_f32_e32 v6, v9, v6
	v_add_f32_e32 v6, v6, v7
	v_med3_f32 v6, v6, s5, v38
	v_med3_f32 v7, v8, s5, v38
	v_mul_f32_e32 v6, 0x3fb8aa3b, v6
	v_mul_f32_e32 v7, 0x3fb8aa3b, v7
	v_exp_f32_e32 v75, v6
	v_exp_f32_e32 v76, v7
	ds_read_b128 v[6:9], v19 offset:9024
	ds_read_b128 v[14:17], v19 offset:10048
	ds_read_b128 v[78:81], v19 offset:9040
	v_cvt_pk_bf16_f32 v77, v75, s0
	global_store_short v[28:29], v77, off offset:1536
	s_waitcnt lgkmcnt(2)
	v_fma_f32 v77, v13, v6, v42
	v_fmac_f32_e32 v77, v10, v7
	ds_read_b128 v[82:85], v19 offset:10064
	v_fmac_f32_e32 v77, v2, v8
	s_waitcnt lgkmcnt(2)
	v_fma_f32 v86, v5, v14, v40
	v_fmac_f32_e32 v77, v3, v9
	v_fmac_f32_e32 v86, v11, v15
	ds_read_b128 v[6:9], v19 offset:9056
	s_waitcnt lgkmcnt(2)
	v_fmac_f32_e32 v77, v57, v78
	v_fmac_f32_e32 v86, v4, v16
	v_fmac_f32_e32 v77, v49, v79
	v_fmac_f32_e32 v86, v12, v17
	v_fmac_f32_e32 v77, v50, v80
	ds_read_b128 v[14:17], v19 offset:10080
	v_fmac_f32_e32 v77, v44, v81
	ds_read_b128 v[78:81], v19 offset:9072
	s_waitcnt lgkmcnt(3)
	v_fmac_f32_e32 v86, v51, v82
	v_fmac_f32_e32 v86, v56, v83
	v_fmac_f32_e32 v86, v54, v84
	s_waitcnt lgkmcnt(2)
	v_fmac_f32_e32 v77, v53, v6
	v_fmac_f32_e32 v86, v52, v85
	v_fmac_f32_e32 v77, v43, v7
	v_pk_mul_f32 v[6:7], v[30:31], v[8:9]
	ds_read_b128 v[82:85], v19 offset:10096
	s_waitcnt lgkmcnt(2)
	v_fmac_f32_e32 v86, v45, v14
	v_add_f32_e32 v6, v77, v6
	v_fmac_f32_e32 v86, v46, v15
	v_add_f32_e32 v8, v6, v7
	v_pk_mul_f32 v[6:7], v[34:35], v[16:17]
	s_nop 0
	v_add_f32_e32 v6, v86, v6
	v_add_f32_e32 v9, v6, v7
	s_waitcnt lgkmcnt(1)
	v_pk_mul_f32 v[6:7], v[32:33], v[78:79]
	s_nop 0
	v_add_f32_e32 v6, v8, v6
	v_add_f32_e32 v8, v6, v7
	s_waitcnt lgkmcnt(0)
	v_pk_mul_f32 v[6:7], v[22:23], v[82:83]
	s_nop 0
	v_add_f32_e32 v6, v9, v6
	v_add_f32_e32 v9, v6, v7
	v_pk_mul_f32 v[6:7], v[20:21], v[80:81]
	s_nop 0
	v_add_f32_e32 v6, v8, v6
	v_add_f32_e32 v8, v6, v7
	v_pk_mul_f32 v[6:7], v[24:25], v[84:85]
	s_nop 0
	v_add_f32_e32 v6, v9, v6
	v_add_f32_e32 v6, v6, v7
	v_med3_f32 v6, v6, s5, v38
	v_mul_f32_e32 v6, 0x3fb8aa3b, v6
	v_med3_f32 v7, v8, s5, v38
	v_exp_f32_e32 v77, v6
	v_mul_f32_e32 v6, 0x3fb8aa3b, v7
	v_exp_f32_e32 v78, v6
	ds_read_b128 v[6:9], v19 offset:9088
	v_cvt_pk_bf16_f32 v14, v77, s0
	global_store_short v[28:29], v14, off offset:1664
	ds_read_b128 v[14:17], v19 offset:9104
	ds_read_b128 v[80:83], v19 offset:10112
	s_waitcnt lgkmcnt(2)
	v_fma_f32 v79, v13, v6, v42
	v_fmac_f32_e32 v79, v10, v7
	v_fmac_f32_e32 v79, v2, v8
	v_fmac_f32_e32 v79, v3, v9
	ds_read_b128 v[6:9], v19 offset:10128
	s_waitcnt lgkmcnt(1)
	v_fma_f32 v86, v5, v80, v40
	v_fmac_f32_e32 v86, v11, v81
	v_fmac_f32_e32 v79, v57, v14
	v_fmac_f32_e32 v86, v4, v82
	v_fmac_f32_e32 v79, v49, v15
	v_fmac_f32_e32 v86, v12, v83
	v_fmac_f32_e32 v79, v50, v16
	v_fmac_f32_e32 v79, v44, v17
	ds_read_b128 v[14:17], v19 offset:9120
	s_waitcnt lgkmcnt(1)
	v_fmac_f32_e32 v86, v51, v6
	v_fmac_f32_e32 v86, v56, v7
	v_fmac_f32_e32 v86, v54, v8
	v_fmac_f32_e32 v86, v52, v9
	ds_read_b128 v[6:9], v19 offset:10144
	ds_read_b128 v[80:83], v19 offset:9136
	s_waitcnt lgkmcnt(2)
	v_fmac_f32_e32 v79, v53, v14
	v_fmac_f32_e32 v79, v43, v15
	v_pk_mul_f32 v[84:85], v[30:31], v[16:17]
	ds_read_b128 v[14:17], v19 offset:10160
	s_waitcnt lgkmcnt(2)
	v_fmac_f32_e32 v86, v45, v6
	v_add_f32_e32 v6, v79, v84
	v_fmac_f32_e32 v86, v46, v7
	v_add_f32_e32 v79, v6, v85
	v_pk_mul_f32 v[6:7], v[34:35], v[8:9]
	s_nop 0
	v_add_f32_e32 v6, v86, v6
	v_add_f32_e32 v8, v6, v7
	s_waitcnt lgkmcnt(1)
	v_pk_mul_f32 v[6:7], v[32:33], v[80:81]
	ds_read_b128 v[86:89], v19 offset:10176
	v_add_f32_e32 v6, v79, v6
	v_add_f32_e32 v9, v6, v7
	s_waitcnt lgkmcnt(1)
	v_pk_mul_f32 v[6:7], v[22:23], v[14:15]
	s_waitcnt lgkmcnt(0)
	v_fmac_f32_e32 v40, v5, v86
	v_add_f32_e32 v6, v8, v6
	v_add_f32_e32 v8, v6, v7
	v_pk_mul_f32 v[6:7], v[20:21], v[82:83]
	ds_read_b128 v[82:85], v19 offset:9152
	v_add_f32_e32 v6, v9, v6
	v_add_f32_e32 v9, v6, v7
	v_pk_mul_f32 v[6:7], v[24:25], v[16:17]
	ds_read_b128 v[14:17], v19 offset:10192
	v_add_f32_e32 v6, v8, v6
	v_add_f32_e32 v6, v6, v7
	v_med3_f32 v6, v6, s5, v38
	v_mul_f32_e32 v6, 0x3fb8aa3b, v6
	v_exp_f32_e32 v79, v6
	v_med3_f32 v7, v9, s5, v38
	v_mul_f32_e32 v7, 0x3fb8aa3b, v7
	v_exp_f32_e32 v80, v7
	v_cvt_pk_bf16_f32 v6, v79, s0
	global_store_short v[28:29], v6, off offset:1792
	ds_read_b128 v[6:9], v19 offset:9168
	s_waitcnt lgkmcnt(2)
	v_fmac_f32_e32 v42, v13, v82
	v_fmac_f32_e32 v42, v10, v83
	v_fmac_f32_e32 v40, v11, v87
	v_fmac_f32_e32 v42, v2, v84
	v_fmac_f32_e32 v42, v3, v85
	v_fmac_f32_e32 v40, v4, v88
	v_fmac_f32_e32 v40, v12, v89
	ds_read_b128 v[10:13], v19 offset:9184
	ds_read_b128 v[2:5], v19 offset:9200
	s_waitcnt lgkmcnt(2)
	v_fmac_f32_e32 v42, v57, v6
	v_fmac_f32_e32 v42, v49, v7
	ds_read_b128 v[82:85], v19 offset:10208
	v_fmac_f32_e32 v40, v51, v14
	v_fmac_f32_e32 v42, v50, v8
	v_fmac_f32_e32 v40, v56, v15
	v_fmac_f32_e32 v42, v44, v9
	v_fmac_f32_e32 v40, v54, v16
	s_waitcnt lgkmcnt(2)
	v_fmac_f32_e32 v42, v53, v10
	ds_read_b128 v[6:9], v19 offset:10224
	v_fmac_f32_e32 v40, v52, v17
	v_fmac_f32_e32 v42, v43, v11
	v_pk_mul_f32 v[10:11], v[30:31], v[12:13]
	s_waitcnt lgkmcnt(1)
	v_fmac_f32_e32 v40, v45, v82
	v_add_f32_e32 v10, v42, v10
	v_fmac_f32_e32 v40, v46, v83
	v_add_f32_e32 v12, v10, v11
	v_pk_mul_f32 v[10:11], v[34:35], v[84:85]
	v_pk_mul_f32 v[2:3], v[32:33], v[2:3]
	v_add_f32_e32 v10, v40, v10
	v_add_f32_e32 v2, v12, v2
	v_add_f32_e32 v10, v10, v11
	v_add_f32_e32 v11, v2, v3
	s_waitcnt lgkmcnt(0)
	v_pk_mul_f32 v[2:3], v[22:23], v[6:7]
	s_nop 0
	v_add_f32_e32 v2, v10, v2
	v_add_f32_e32 v6, v2, v3
	v_pk_mul_f32 v[2:3], v[20:21], v[4:5]
	v_cvt_pk_bf16_f32 v5, v64, v66
	v_add_f32_e32 v2, v11, v2
	v_add_f32_e32 v4, v2, v3
	v_pk_mul_f32 v[2:3], v[24:25], v[8:9]
	s_nop 0
	v_add_f32_e32 v2, v6, v2
	v_add_f32_e32 v2, v2, v3
	v_med3_f32 v2, v2, s5, v38
	v_mul_f32_e32 v2, 0x3fb8aa3b, v2
	v_exp_f32_e32 v10, v2
	v_med3_f32 v2, v4, s5, v38
	v_mul_f32_e32 v2, 0x3fb8aa3b, v2
	v_exp_f32_e32 v11, v2
	v_cvt_pk_bf16_f32 v2, v10, s0
	global_store_short v[28:29], v2, off offset:1920
	v_lshlrev_b32_e32 v2, 7, v36
	v_or3_b32 v26, v2, s4, v26
	v_lshl_add_u64 v[6:7], s[12:13], 0, v[26:27]
	v_cvt_pk_bf16_f32 v2, v37, v41
	v_cvt_pk_bf16_f32 v3, v48, v58
	v_cvt_pk_bf16_f32 v4, v60, v62
	global_store_dwordx4 v[6:7], v[2:5], off
	v_lshl_add_u64 v[8:9], s[14:15], 0, v[26:27]
	s_mov_b64 s[4:5], 0
	v_cvt_pk_bf16_f32 v2, v68, v70
	v_cvt_pk_bf16_f32 v3, v72, v74
	v_cvt_pk_bf16_f32 v4, v76, v78
	v_cvt_pk_bf16_f32 v5, v80, v11
	global_store_dwordx4 v[6:7], v[2:5], off offset:16
	s_nop 1
	v_cvt_pk_bf16_f32 v2, v18, v39
	v_cvt_pk_bf16_f32 v3, v47, v55
	v_cvt_pk_bf16_f32 v4, v59, v61
	v_cvt_pk_bf16_f32 v5, v63, v65
	global_store_dwordx4 v[8:9], v[2:5], off
	s_nop 1
	v_cvt_pk_bf16_f32 v2, v67, v69
	v_cvt_pk_bf16_f32 v3, v71, v73
	v_cvt_pk_bf16_f32 v4, v75, v77
	v_cvt_pk_bf16_f32 v5, v79, v10
	global_store_dwordx4 v[8:9], v[2:5], off offset:16

	.amdhsa_kernel _Z11prep_kernelPKfS0_S0_S0_S0_S0_S0_S0_S0_S0_S0_S0_PtS1_S1_S1_S1_S1_
		.amdhsa_group_segment_fixed_size 16640
		.amdhsa_private_segment_fixed_size 0
		.amdhsa_kernarg_size 144
		.amdhsa_user_sgpr_count 2
		.amdhsa_user_sgpr_dispatch_ptr 0
		.amdhsa_user_sgpr_queue_ptr 0
		.amdhsa_user_sgpr_kernarg_segment_ptr 1
		.amdhsa_user_sgpr_dispatch_id 0
		.amdhsa_user_sgpr_kernarg_preload_length 0
		.amdhsa_user_sgpr_kernarg_preload_offset 0
		.amdhsa_user_sgpr_private_segment_size 0
		.amdhsa_uses_dynamic_stack 0
		.amdhsa_enable_private_segment 0
		.amdhsa_system_sgpr_workgroup_id_x 1
		.amdhsa_system_sgpr_workgroup_id_y 0
		.amdhsa_system_sgpr_workgroup_id_z 0
		.amdhsa_system_sgpr_workgroup_info 0
		.amdhsa_system_vgpr_workitem_id 0
		.amdhsa_next_free_vgpr 168
		.amdhsa_next_free_sgpr 40
		.amdhsa_accum_offset 156
		.amdhsa_reserve_vcc 1
		.amdhsa_float_round_mode_32 0
		.amdhsa_float_round_mode_16_64 0
		.amdhsa_float_denorm_mode_32 3
		.amdhsa_float_denorm_mode_16_64 3
		.amdhsa_dx10_clamp 1
		.amdhsa_ieee_mode 1
		.amdhsa_fp16_overflow 0
		.amdhsa_tg_split 0
		.amdhsa_exception_fp_ieee_invalid_op 0
		.amdhsa_exception_fp_denorm_src 0
		.amdhsa_exception_fp_ieee_div_zero 0
		.amdhsa_exception_fp_ieee_overflow 0
		.amdhsa_exception_fp_ieee_underflow 0
		.amdhsa_exception_fp_ieee_inexact 0
		.amdhsa_exception_int_div_zero 0
	.end_amdhsa_kernel

amdhsa.kernels:
  - .agpr_count:     0
    .args:
      - .actual_access:  read_only
        .address_space:  global
        .offset:         0
        .size:           8
        .value_kind:     global_buffer
      - .actual_access:  read_only
        .address_space:  global
        .offset:         8
        .size:           8
        .value_kind:     global_buffer
      - .actual_access:  write_only
        .address_space:  global
        .offset:         16
        .size:           8
        .value_kind:     global_buffer
      - .offset:         24
        .size:           4
        .value_kind:     by_value
      - .offset:         28
        .size:           4
        .value_kind:     by_value
      - .offset:         32
        .size:           4
        .value_kind:     by_value
      - .offset:         36
        .size:           4
        .value_kind:     by_value
    .group_segment_fixed_size: 8256
    .kernarg_segment_align: 8
    .kernarg_segment_size: 40
    .language:       OpenCL C
    .language_version:
      - 2
      - 0
    .max_flat_workgroup_size: 256
    .name:           _Z14gemm_f32_naivePKfS0_Pfiiii
    .private_segment_fixed_size: 0
    .sgpr_count:     24
    .sgpr_spill_count: 0
    .symbol:         _Z14gemm_f32_naivePKfS0_Pfiiii.kd
    .uniform_work_group_size: 1
    .uses_dynamic_stack: false
    .vgpr_count:     76
    .vgpr_spill_count: 0
    .wavefront_size: 64
  - .agpr_count:     0
    .args:
      - .actual_access:  read_only
        .address_space:  global
        .offset:         0
        .size:           8
        .value_kind:     global_buffer
      - .actual_access:  write_only
        .address_space:  global
        .offset:         8
        .size:           8
        .value_kind:     global_buffer
      - .actual_access:  write_only
        .address_space:  global
        .offset:         16
        .size:           8
        .value_kind:     global_buffer
      - .actual_access:  write_only
        .address_space:  global
        .offset:         24
        .size:           8
        .value_kind:     global_buffer
      - .actual_access:  write_only
        .address_space:  global
        .offset:         32
        .size:           8
        .value_kind:     global_buffer
      - .actual_access:  write_only
        .address_space:  global
        .offset:         40
        .size:           8
        .value_kind:     global_buffer
      - .actual_access:  write_only
        .address_space:  global
        .offset:         48
        .size:           8
        .value_kind:     global_buffer
    .group_segment_fixed_size: 0
    .kernarg_segment_align: 8
    .kernarg_segment_size: 56
    .language:       OpenCL C
    .language_version:
      - 2
      - 0
    .max_flat_workgroup_size: 256
    .name:           _Z10post_naivePKfPtS1_S1_S1_S1_S1_
    .private_segment_fixed_size: 0
    .sgpr_count:     28
    .sgpr_spill_count: 0
    .symbol:         _Z10post_naivePKfPtS1_S1_S1_S1_S1_.kd
    .uniform_work_group_size: 1
    .uses_dynamic_stack: false
    .vgpr_count:     38
    .vgpr_spill_count: 0
    .wavefront_size: 64
  - .agpr_count:     0
    .args:
      - .actual_access:  read_only
        .address_space:  global
        .offset:         0
        .size:           8
        .value_kind:     global_buffer
      - .actual_access:  read_only
        .address_space:  global
        .offset:         8
        .size:           8
        .value_kind:     global_buffer
      - .actual_access:  read_only
        .address_space:  global
        .offset:         16
        .size:           8
        .value_kind:     global_buffer
      - .actual_access:  read_only
        .address_space:  global
        .offset:         24
        .size:           8
        .value_kind:     global_buffer
      - .actual_access:  read_only
        .address_space:  global
        .offset:         32
        .size:           8
        .value_kind:     global_buffer
      - .actual_access:  read_only
        .address_space:  global
        .offset:         40
        .size:           8
        .value_kind:     global_buffer
      - .actual_access:  read_only
        .address_space:  global
        .offset:         48
        .size:           8
        .value_kind:     global_buffer
      - .actual_access:  write_only
        .address_space:  global
        .offset:         56
        .size:           8
        .value_kind:     global_buffer
      - .actual_access:  write_only
        .address_space:  global
        .offset:         64
        .size:           8
        .value_kind:     global_buffer
      - .actual_access:  write_only
        .address_space:  global
        .offset:         72
        .size:           8
        .value_kind:     global_buffer
      - .actual_access:  write_only
        .address_space:  global
        .offset:         80
        .size:           8
        .value_kind:     global_buffer
    .group_segment_fixed_size: 1152
    .kernarg_segment_align: 8
    .kernarg_segment_size: 88
    .language:       OpenCL C
    .language_version:
      - 2
      - 0
    .max_flat_workgroup_size: 256
    .name:           _Z11gates_naivePKfS0_S0_S0_S0_S0_S0_PtS1_S1_S1_
    .private_segment_fixed_size: 0
    .sgpr_count:     32
    .sgpr_spill_count: 0
    .symbol:         _Z11gates_naivePKfS0_S0_S0_S0_S0_S0_PtS1_S1_S1_.kd
    .uniform_work_group_size: 1
    .uses_dynamic_stack: false
    .vgpr_count:     66
    .vgpr_spill_count: 0
    .wavefront_size: 64
  - .agpr_count:     0
    .args:
      - .actual_access:  read_only
        .address_space:  global
        .offset:         0
        .size:           8
        .value_kind:     global_buffer
      - .actual_access:  read_only
        .address_space:  global
        .offset:         8
        .size:           8
        .value_kind:     global_buffer
      - .actual_access:  read_only
        .address_space:  global
        .offset:         16
        .size:           8
        .value_kind:     global_buffer
      - .actual_access:  read_only
        .address_space:  global
        .offset:         24
        .size:           8
        .value_kind:     global_buffer
      - .actual_access:  read_only
        .address_space:  global
        .offset:         32
        .size:           8
        .value_kind:     global_buffer
      - .actual_access:  read_only
        .address_space:  global
        .offset:         40
        .size:           8
        .value_kind:     global_buffer
      - .actual_access:  read_only
        .address_space:  global
        .offset:         48
        .size:           8
        .value_kind:     global_buffer
      - .actual_access:  write_only
        .address_space:  global
        .offset:         56
        .size:           8
        .value_kind:     global_buffer
    .group_segment_fixed_size: 12560
    .kernarg_segment_align: 8
    .kernarg_segment_size: 64
    .language:       OpenCL C
    .language_version:
      - 2
      - 0
    .max_flat_workgroup_size: 256
    .name:           _Z10attn_naivePKtS0_S0_S0_S0_S0_PKfPf
    .private_segment_fixed_size: 0
    .sgpr_count:     33
    .sgpr_spill_count: 0
    .symbol:         _Z10attn_naivePKtS0_S0_S0_S0_S0_PKfPf.kd
    .uniform_work_group_size: 1
    .uses_dynamic_stack: false
    .vgpr_count:     82
    .vgpr_spill_count: 0
    .wavefront_size: 64
  - .agpr_count:     0
    .args:
      - .address_space:  global
        .offset:         0
        .size:           8
        .value_kind:     global_buffer
      - .address_space:  global
        .offset:         8
        .size:           8
        .value_kind:     global_buffer
      - .actual_access:  write_only
        .address_space:  global
        .offset:         16
        .size:           8
        .value_kind:     global_buffer
    .group_segment_fixed_size: 0
    .kernarg_segment_align: 8
    .kernarg_segment_size: 24
    .language:       OpenCL C
    .language_version:
      - 2
      - 0
    .max_flat_workgroup_size: 512
    .name:           _Z8gemm_outPKtS0_Pf
    .private_segment_fixed_size: 0
    .sgpr_count:     26
    .sgpr_spill_count: 0
    .symbol:         _Z8gemm_outPKtS0_Pf.kd
    .uniform_work_group_size: 1
    .uses_dynamic_stack: false
    .vgpr_count:     158
    .vgpr_spill_count: 0
    .wavefront_size: 64
  - .agpr_count:     0
    .args:
      - .address_space:  global
        .offset:         0
        .size:           8
        .value_kind:     global_buffer
      - .address_space:  global
        .offset:         8
        .size:           8
        .value_kind:     global_buffer
      - .actual_access:  write_only
        .address_space:  global
        .offset:         16
        .size:           8
        .value_kind:     global_buffer
    .group_segment_fixed_size: 0
    .kernarg_segment_align: 8
    .kernarg_segment_size: 24
    .language:       OpenCL C
    .language_version:
      - 2
      - 0
    .max_flat_workgroup_size: 512
    .name:           _Z9gemm_out2PKtS0_Pf
    .private_segment_fixed_size: 0
    .sgpr_count:     27
    .sgpr_spill_count: 0
    .symbol:         _Z9gemm_out2PKtS0_Pf.kd
    .uniform_work_group_size: 1
    .uses_dynamic_stack: false
    .vgpr_count:     146
    .vgpr_spill_count: 0
    .wavefront_size: 64
  - .agpr_count:     0
    .args:
      - .actual_access:  read_only
        .address_space:  global
        .offset:         0
        .size:           8
        .value_kind:     global_buffer
      - .actual_access:  write_only
        .address_space:  global
        .offset:         8
        .size:           8
        .value_kind:     global_buffer
    .group_segment_fixed_size: 0
    .kernarg_segment_align: 8
    .kernarg_segment_size: 16
    .language:       OpenCL C
    .language_version:
      - 2
      - 0
    .max_flat_workgroup_size: 256
    .name:           _Z6conv_xPKfPt
    .private_segment_fixed_size: 0
    .sgpr_count:     14
    .sgpr_spill_count: 0
    .symbol:         _Z6conv_xPKfPt.kd
    .uniform_work_group_size: 1
    .uses_dynamic_stack: false
    .vgpr_count:     12
    .vgpr_spill_count: 0
    .wavefront_size: 64
  - .agpr_count:     0
    .args:
      - .actual_access:  read_only
        .address_space:  global
        .offset:         0
        .size:           8
        .value_kind:     global_buffer
      - .actual_access:  read_only
        .address_space:  global
        .offset:         8
        .size:           8
        .value_kind:     global_buffer
      - .actual_access:  read_only
        .address_space:  global
        .offset:         16
        .size:           8
        .value_kind:     global_buffer
      - .actual_access:  read_only
        .address_space:  global
        .offset:         24
        .size:           8
        .value_kind:     global_buffer
      - .actual_access:  read_only
        .address_space:  global
        .offset:         32
        .size:           8
        .value_kind:     global_buffer
      - .actual_access:  write_only
        .address_space:  global
        .offset:         40
        .size:           8
        .value_kind:     global_buffer
      - .actual_access:  write_only
        .address_space:  global
        .offset:         48
        .size:           8
        .value_kind:     global_buffer
    .group_segment_fixed_size: 16640
    .kernarg_segment_align: 8
    .kernarg_segment_size: 56
    .language:       OpenCL C
    .language_version:
      - 2
      - 0
    .max_flat_workgroup_size: 256
    .name:           _Z7conv_wTPKfS0_S0_S0_S0_PtS1_
    .private_segment_fixed_size: 0
    .sgpr_count:     26
    .sgpr_spill_count: 0
    .symbol:         _Z7conv_wTPKfS0_S0_S0_S0_PtS1_.kd
    .uniform_work_group_size: 1
    .uses_dynamic_stack: false
    .vgpr_count:     51
    .vgpr_spill_count: 0
    .wavefront_size: 64
  - .agpr_count:     0
    .args:
      - .actual_access:  read_only
        .address_space:  global
        .offset:         0
        .size:           8
        .value_kind:     global_buffer
      - .actual_access:  read_only
        .address_space:  global
        .offset:         8
        .size:           8
        .value_kind:     global_buffer
      - .actual_access:  write_only
        .address_space:  global
        .offset:         16
        .size:           8
        .value_kind:     global_buffer
    .group_segment_fixed_size: 0
    .kernarg_segment_align: 8
    .kernarg_segment_size: 24
    .language:       OpenCL C
    .language_version:
      - 2
      - 0
    .max_flat_workgroup_size: 256
    .name:           _Z7conv_w1PKfS0_Pt
    .private_segment_fixed_size: 0
    .sgpr_count:     16
    .sgpr_spill_count: 0
    .symbol:         _Z7conv_w1PKfS0_Pt.kd
    .uniform_work_group_size: 1
    .uses_dynamic_stack: false
    .vgpr_count:     6
    .vgpr_spill_count: 0
    .wavefront_size: 64
  - .agpr_count:     8
    .args:
      - .actual_access:  read_only
        .address_space:  global
        .offset:         0
        .size:           8
        .value_kind:     global_buffer
      - .actual_access:  read_only
        .address_space:  global
        .offset:         8
        .size:           8
        .value_kind:     global_buffer
      - .actual_access:  read_only
        .address_space:  global
        .offset:         16
        .size:           8
        .value_kind:     global_buffer
      - .actual_access:  read_only
        .address_space:  global
        .offset:         24
        .size:           8
        .value_kind:     global_buffer
      - .actual_access:  read_only
        .address_space:  global
        .offset:         32
        .size:           8
        .value_kind:     global_buffer
      - .actual_access:  read_only
        .address_space:  global
        .offset:         40
        .size:           8
        .value_kind:     global_buffer
      - .actual_access:  write_only
        .address_space:  global
        .offset:         48
        .size:           8
        .value_kind:     global_buffer
      - .actual_access:  write_only
        .address_space:  global
        .offset:         56
        .size:           8
        .value_kind:     global_buffer
      - .actual_access:  write_only
        .address_space:  global
        .offset:         64
        .size:           8
        .value_kind:     global_buffer
    .group_segment_fixed_size: 10240
    .kernarg_segment_align: 8
    .kernarg_segment_size: 72
    .language:       OpenCL C
    .language_version:
      - 2
      - 0
    .max_flat_workgroup_size: 256
    .name:           _Z10gates_fastPKtS0_PKfS2_S2_S2_PtS3_S3_
    .private_segment_fixed_size: 0
    .sgpr_count:     24
    .sgpr_spill_count: 0
    .symbol:         _Z10gates_fastPKtS0_PKfS2_S2_S2_PtS3_S3_.kd
    .uniform_work_group_size: 1
    .uses_dynamic_stack: false
    .vgpr_count:     96
    .vgpr_spill_count: 0
    .wavefront_size: 64
  - .agpr_count:     4
    .args:
      - .actual_access:  read_only
        .address_space:  global
        .offset:         0
        .size:           8
        .value_kind:     global_buffer
      - .actual_access:  read_only
        .address_space:  global
        .offset:         8
        .size:           8
        .value_kind:     global_buffer
      - .actual_access:  read_only
        .address_space:  global
        .offset:         16
        .size:           8
        .value_kind:     global_buffer
      - .actual_access:  read_only
        .address_space:  global
        .offset:         24
        .size:           8
        .value_kind:     global_buffer
      - .actual_access:  write_only
        .address_space:  global
        .offset:         32
        .size:           8
        .value_kind:     global_buffer
      - .actual_access:  write_only
        .address_space:  global
        .offset:         40
        .size:           8
        .value_kind:     global_buffer
      - .actual_access:  write_only
        .address_space:  global
        .offset:         48
        .size:           8
        .value_kind:     global_buffer
    .group_segment_fixed_size: 0
    .kernarg_segment_align: 8
    .kernarg_segment_size: 56
    .language:       OpenCL C
    .language_version:
      - 2
      - 0
    .max_flat_workgroup_size: 256
    .name:           _Z10state_fastPKtS0_S0_S0_PtS1_Pf
    .private_segment_fixed_size: 0
    .sgpr_count:     20
    .sgpr_spill_count: 0
    .symbol:         _Z10state_fastPKtS0_S0_S0_PtS1_Pf.kd
    .uniform_work_group_size: 1
    .uses_dynamic_stack: false
    .vgpr_count:     184
    .vgpr_spill_count: 0
    .wavefront_size: 64
  - .agpr_count:     0
    .args:
      - .actual_access:  read_only
        .address_space:  global
        .offset:         0
        .size:           8
        .value_kind:     global_buffer
      - .actual_access:  read_only
        .address_space:  global
        .offset:         8
        .size:           8
        .value_kind:     global_buffer
      - .actual_access:  read_only
        .address_space:  global
        .offset:         16
        .size:           8
        .value_kind:     global_buffer
      - .actual_access:  write_only
        .address_space:  global
        .offset:         24
        .size:           8
        .value_kind:     global_buffer
      - .actual_access:  write_only
        .address_space:  global
        .offset:         32
        .size:           8
        .value_kind:     global_buffer
      - .actual_access:  write_only
        .address_space:  global
        .offset:         40
        .size:           8
        .value_kind:     global_buffer
    .group_segment_fixed_size: 0
    .kernarg_segment_align: 8
    .kernarg_segment_size: 48
    .language:       OpenCL C
    .language_version:
      - 2
      - 0
    .max_flat_workgroup_size: 256
    .name:           _Z11prefix_fastPKtS0_PKfPtS3_Pf
    .private_segment_fixed_size: 0
    .sgpr_count:     106
    .sgpr_spill_count: 41
    .symbol:         _Z11prefix_fastPKtS0_PKfPtS3_Pf.kd
    .uniform_work_group_size: 1
    .uses_dynamic_stack: false
    .vgpr_count:     205
    .vgpr_spill_count: 0
    .wavefront_size: 64
  - .agpr_count:     0
    .args:
      - .address_space:  global
        .offset:         0
        .size:           8
        .value_kind:     global_buffer
      - .address_space:  global
        .offset:         8
        .size:           8
        .value_kind:     global_buffer
      - .address_space:  global
        .offset:         16
        .size:           8
        .value_kind:     global_buffer
      - .actual_access:  read_only
        .address_space:  global
        .offset:         24
        .size:           8
        .value_kind:     global_buffer
      - .address_space:  global
        .offset:         32
        .size:           8
        .value_kind:     global_buffer
      - .address_space:  global
        .offset:         40
        .size:           8
        .value_kind:     global_buffer
      - .address_space:  global
        .offset:         48
        .size:           8
        .value_kind:     global_buffer
      - .address_space:  global
        .offset:         56
        .size:           8
        .value_kind:     global_buffer
      - .address_space:  global
        .offset:         64
        .size:           8
        .value_kind:     global_buffer
      - .address_space:  global
        .offset:         72
        .size:           8
        .value_kind:     global_buffer
      - .address_space:  global
        .offset:         80
        .size:           8
        .value_kind:     global_buffer
      - .actual_access:  write_only
        .address_space:  global
        .offset:         88
        .size:           8
        .value_kind:     global_buffer
    .group_segment_fixed_size: 0
    .kernarg_segment_align: 8
    .kernarg_segment_size: 96
    .language:       OpenCL C
    .language_version:
      - 2
      - 0
    .max_flat_workgroup_size: 512
    .name:           _Z9attn_fastPKtS0_S0_S0_S0_S0_S0_S0_S0_PKfS2_Pt
    .private_segment_fixed_size: 0
    .sgpr_count:     52
    .sgpr_spill_count: 0
    .symbol:         _Z9attn_fastPKtS0_S0_S0_S0_S0_S0_S0_S0_PKfS2_Pt.kd
    .uniform_work_group_size: 1
    .uses_dynamic_stack: false
    .vgpr_count:     224
    .vgpr_spill_count: 0
    .wavefront_size: 64
  - .agpr_count:     12
    .args:
      - .actual_access:  read_only
        .address_space:  global
        .offset:         0
        .size:           8
        .value_kind:     global_buffer
      - .actual_access:  read_only
        .address_space:  global
        .offset:         8
        .size:           8
        .value_kind:     global_buffer
      - .actual_access:  read_only
        .address_space:  global
        .offset:         16
        .size:           8
        .value_kind:     global_buffer
      - .actual_access:  read_only
        .address_space:  global
        .offset:         24
        .size:           8
        .value_kind:     global_buffer
      - .actual_access:  read_only
        .address_space:  global
        .offset:         32
        .size:           8
        .value_kind:     global_buffer
      - .actual_access:  read_only
        .address_space:  global
        .offset:         40
        .size:           8
        .value_kind:     global_buffer
      - .actual_access:  read_only
        .address_space:  global
        .offset:         48
        .size:           8
        .value_kind:     global_buffer
      - .actual_access:  read_only
        .address_space:  global
        .offset:         56
        .size:           8
        .value_kind:     global_buffer
      - .actual_access:  read_only
        .address_space:  global
        .offset:         64
        .size:           8
        .value_kind:     global_buffer
      - .actual_access:  read_only
        .address_space:  global
        .offset:         72
        .size:           8
        .value_kind:     global_buffer
      - .actual_access:  read_only
        .address_space:  global
        .offset:         80
        .size:           8
        .value_kind:     global_buffer
      - .actual_access:  read_only
        .address_space:  global
        .offset:         88
        .size:           8
        .value_kind:     global_buffer
      - .actual_access:  write_only
        .address_space:  global
        .offset:         96
        .size:           8
        .value_kind:     global_buffer
      - .actual_access:  write_only
        .address_space:  global
        .offset:         104
        .size:           8
        .value_kind:     global_buffer
      - .actual_access:  write_only
        .address_space:  global
        .offset:         112
        .size:           8
        .value_kind:     global_buffer
      - .actual_access:  write_only
        .address_space:  global
        .offset:         120
        .size:           8
        .value_kind:     global_buffer
      - .actual_access:  write_only
        .address_space:  global
        .offset:         128
        .size:           8
        .value_kind:     global_buffer
      - .actual_access:  write_only
        .address_space:  global
        .offset:         136
        .size:           8
        .value_kind:     global_buffer
    .group_segment_fixed_size: 16640
    .kernarg_segment_align: 8
    .kernarg_segment_size: 144
    .language:       OpenCL C
    .language_version:
      - 2
      - 0
    .max_flat_workgroup_size: 256
    .name:           _Z11prep_kernelPKfS0_S0_S0_S0_S0_S0_S0_S0_S0_S0_S0_PtS1_S1_S1_S1_S1_
    .private_segment_fixed_size: 0
    .sgpr_count:     46
    .sgpr_spill_count: 0
    .symbol:         _Z11prep_kernelPKfS0_S0_S0_S0_S0_S0_S0_S0_S0_S0_S0_PtS1_S1_S1_S1_S1_.kd
    .uniform_work_group_size: 1
    .uses_dynamic_stack: false
    .vgpr_count:     168
    .vgpr_spill_count: 0
    .wavefront_size: 64
  - .agpr_count:     0
    .args:
      - .address_space:  global
        .offset:         0
        .size:           8
        .value_kind:     global_buffer
      - .address_space:  global
        .offset:         8
        .size:           8
        .value_kind:     global_buffer
      - .offset:         16
        .size:           4
        .value_kind:     by_value
      - .offset:         20
        .size:           4
        .value_kind:     by_value
      - .offset:         24
        .size:           4
        .value_kind:     by_value
      - .offset:         28
        .size:           4
        .value_kind:     by_value
      - .address_space:  global
        .offset:         32
        .size:           8
        .value_kind:     global_buffer
    .group_segment_fixed_size: 0
    .kernarg_segment_align: 8
    .kernarg_segment_size: 40
    .language:       OpenCL C
    .language_version:
      - 2
      - 0
    .max_flat_workgroup_size: 1024
    .name:           _Z9dbg_cmp16PKtS0_iiffPf
    .private_segment_fixed_size: 0
    .sgpr_count:     18
    .sgpr_spill_count: 0
    .symbol:         _Z9dbg_cmp16PKtS0_iiffPf.kd
    .uniform_work_group_size: 1
    .uses_dynamic_stack: false
    .vgpr_count:     5
    .vgpr_spill_count: 0
    .wavefront_size: 64
  - .agpr_count:     0
    .args:
      - .address_space:  global
        .offset:         0
        .size:           8
        .value_kind:     global_buffer
      - .address_space:  global
        .offset:         8
        .size:           8
        .value_kind:     global_buffer
      - .offset:         16
        .size:           4
        .value_kind:     by_value
      - .offset:         20
        .size:           4
        .value_kind:     by_value
      - .offset:         24
        .size:           56
        .value_kind:     by_value
    .group_segment_fixed_size: 0
    .kernarg_segment_align: 8
    .kernarg_segment_size: 80
    .language:       OpenCL C
    .language_version:
      - 2
      - 0
    .max_flat_workgroup_size: 512
    .name:           _Z5gemm8ILi0EEvPKtS1_ii7EpiArgs
    .private_segment_fixed_size: 0
    .sgpr_count:     36
    .sgpr_spill_count: 0
    .symbol:         _Z5gemm8ILi0EEvPKtS1_ii7EpiArgs.kd
    .uniform_work_group_size: 1
    .uses_dynamic_stack: false
    .vgpr_count:     246
    .vgpr_spill_count: 0
    .wavefront_size: 64
  - .agpr_count:     0
    .args:
      - .address_space:  global
        .offset:         0
        .size:           8
        .value_kind:     global_buffer
      - .address_space:  global
        .offset:         8
        .size:           8
        .value_kind:     global_buffer
      - .address_space:  global
        .offset:         16
        .size:           8
        .value_kind:     global_buffer
      - .address_space:  global
        .offset:         24
        .size:           8
        .value_kind:     global_buffer
      - .actual_access:  write_only
        .address_space:  global
        .offset:         32
        .size:           8
        .value_kind:     global_buffer
      - .actual_access:  write_only
        .address_space:  global
        .offset:         40
        .size:           8
        .value_kind:     global_buffer
      - .actual_access:  write_only
        .address_space:  global
        .offset:         48
        .size:           8
        .value_kind:     global_buffer
    .group_segment_fixed_size: 81920
    .kernarg_segment_align: 8
    .kernarg_segment_size: 56
    .language:       OpenCL C
    .language_version:
      - 2
      - 0
    .max_flat_workgroup_size: 256
    .name:           _Z9scan_fastILb1EEvPKtS1_S1_S1_PtS2_Pf
    .private_segment_fixed_size: 0
    .sgpr_count:     62
    .sgpr_spill_count: 0
    .symbol:         _Z9scan_fastILb1EEvPKtS1_S1_S1_PtS2_Pf.kd
    .uniform_work_group_size: 1
    .uses_dynamic_stack: false
    .vgpr_count:     160
    .vgpr_spill_count: 0
    .wavefront_size: 64
